# v3 + MoE meta words fetched together + head-norm gains loaded once per q/k tile (no per-row-group store drain)
# speedup vs baseline: 1.0110x; 1.0070x over previous
; template <int MASK> __device__ __forceinline__ float swz_f(float v) { return __builtin_bit_cast(float, __builtin_amdgcn_ds_swizzle(__builtin_bit_cast(int, v), (MASK << 10) | 0x1f)); }
; __device__ __forceinline__ float sum_x32(float v) { const unsigned u = __builtin_bit_cast(unsigned, v); auto rr = __builtin_amdgcn_permlane32_swap(u, u, false, false); return __builtin_bit_cast(float, (unsigned)rr[0]) + __builtin_bit_cast(float, (unsigned)rr[1]); }
; __device__ __forceinline__ u32x4 pack8(const f32x4 a, const f32x4 b) { u32x4 w; w.x = cvt_pk_bf16(a[0], a[1]); w.y = cvt_pk_bf16(a[2], a[3]); w.z = cvt_pk_bf16(b[0], b[1]); w.w = cvt_pk_bf16(b[2], b[3]); return w; }
;     __device__ __forceinline__ void operator()(const f32x4 (&acc)[2][2][4][2], const Unit& u, int wr, int wc, int fr, int fq) const {
;     ...
;                 if (!GATES && type <= 1) { float ss = 0.f;
; #pragma unroll
;                     for (int bj = 0; bj < 2; ++bj)
; #pragma unroll
;                         for (int n = 0; n < 2; ++n) ss += (v[bj][n][0] * v[bj][n][0] + v[bj][n][1] * v[bj][n][1]) + (v[bj][n][2] * v[bj][n][2] + v[bj][n][3] * v[bj][n][3]);
;                     ss += swz_f<16>(ss); ss = sum_x32(ss);
;                     const float r = __builtin_amdgcn_rsqf(ss * (1.f / 64.f) + EPS) * gsc;
; #pragma unroll
;                     for (int bj = 0; bj < 2; ++bj)
; #pragma unroll
;                         for (int n = 0; n < 2; ++n) v[bj][n] = v[bj][n] * r * *(const f32x4*)(gp + 32 * bj + 4 * n);
;     ...
;                 bf16* rowp = U + (size_t)row * NIN + pn * BM + 64 * wc + 8 * fq;
; #pragma unroll
;                 for (int bj = 0; bj < 2; ++bj) *(u32x4*)(rowp + 32 * bj) = pack8(v[bj][0], v[bj][1]);
.LBB0_269:
	v_lshlrev_b32_e32 v112, 3, v182
	v_ashrrev_i32_e32 v113, 31, v112
	v_mov_b32_e32 v114, 0x3e38aa3b
	v_cndmask_b32_e64 v129, 1.0, v114, s[2:3]
	v_lshl_add_u64 v[114:115], v[112:113], 2, s[6:7]
	s_and_b64 vcc, exec, s[30:31]
	s_cbranch_vccz .LBB0_271
	v_pk_mul_f32 v[144:145], v[152:153], v[152:153]
	v_pk_mul_f32 v[146:147], v[154:155], v[154:155]
	s_nop 0
	v_pk_mov_b32 v[148:149], v[146:147], v[144:145] op_sel:[1,0]
	v_mov_b32_e32 v147, v145
	v_pk_add_f32 v[144:145], v[148:149], v[146:147]
	v_pk_mul_f32 v[146:147], v[122:123], v[122:123]
	v_pk_add_f32 v[144:145], v[144:145], v[144:145] op_sel_hi:[0,1]
	v_pk_mul_f32 v[148:149], v[124:125], v[124:125]
	v_mul_f32_e32 v144, v126, v126
	v_pk_mov_b32 v[150:151], v[148:149], v[146:147] op_sel:[1,0]
	v_mov_b32_e32 v149, v147
	v_pk_add_f32 v[146:147], v[150:151], v[148:149]
	v_pk_fma_f32 v[148:149], v[126:127], v[126:127], v[144:145] op_sel_hi:[1,1,0]
	v_mul_f32_e32 v144, v120, v120
	v_pk_add_f32 v[146:147], v[146:147], v[146:147] op_sel_hi:[0,1]
	v_pk_fma_f32 v[150:151], v[120:121], v[120:121], v[144:145] op_sel_hi:[1,1,0]
	v_mul_f32_e32 v148, v118, v118
	v_mul_f32_e32 v150, v119, v119
	v_mul_f32_e32 v144, v116, v116
	v_mul_f32_e32 v146, v117, v117
	v_pk_add_f32 v[148:149], v[148:149], v[150:151]
	v_pk_add_f32 v[144:145], v[144:145], v[146:147]
	s_nop 0
	v_pk_add_f32 v[144:145], v[148:149], v[144:145]
	s_nop 0
	v_add_f32_e32 v144, v144, v145
	ds_swizzle_b32 v145, v144 offset:swizzle(SWAP,16)
	s_waitcnt lgkmcnt(0)
	v_add_f32_e32 v144, v144, v145
	v_mov_b32_e32 v145, v144
	s_nop 1
	v_permlane32_swap_b32_e32 v144, v145
	v_add_f32_e32 v144, v144, v145
	v_fmamk_f32 v144, v144, 0x3c800000, v230
	v_rsq_f32_e32 v144, v144
	s_nop 0
	v_mul_f32_e32 v160, v129, v144
	v_pk_mul_f32 v[146:147], v[154:155], v[160:161] op_sel_hi:[1,0]
	v_pk_mul_f32 v[144:145], v[152:153], v[160:161] op_sel_hi:[1,0]
	global_load_dwordx4 v[194:197], v[114:115], off
	global_load_dwordx4 v[198:201], v[114:115], off offset:16
	global_load_dwordx4 v[202:205], v[114:115], off offset:128
	global_load_dwordx4 v[206:209], v[114:115], off offset:144
	global_load_dwordx4 v[148:151], v[114:115], off offset:16
	global_load_dwordx4 v[152:155], v[114:115], off
	v_pk_mul_f32 v[124:125], v[124:125], v[160:161] op_sel_hi:[1,0]
	v_pk_mul_f32 v[122:123], v[122:123], v[160:161] op_sel_hi:[1,0]
	v_pk_mul_f32 v[118:119], v[118:119], v[160:161] op_sel_hi:[1,0]
	v_pk_mul_f32 v[116:117], v[116:117], v[160:161] op_sel_hi:[1,0]
	s_waitcnt vmcnt(1)
	v_pk_mul_f32 v[150:151], v[150:151], v[122:123]
	s_waitcnt vmcnt(0)
	v_pk_mul_f32 v[144:145], v[154:155], v[144:145]
	v_pk_mul_f32 v[146:147], v[152:153], v[146:147]
	v_pk_mul_f32 v[148:149], v[148:149], v[124:125]
	v_pk_mul_f32 v[152:153], v[126:127], v[160:161] op_sel_hi:[1,0]
	v_pk_mul_f32 v[154:155], v[120:121], v[160:161] op_sel_hi:[1,0]
	global_load_dwordx4 v[120:123], v[114:115], off offset:144
	global_load_dwordx4 v[124:127], v[114:115], off offset:128
	s_waitcnt vmcnt(1)
	v_pk_mul_f32 v[160:161], v[122:123], v[116:117]
	s_waitcnt vmcnt(0)
	v_pk_mul_f32 v[156:157], v[126:127], v[154:155]
	v_pk_mul_f32 v[158:159], v[124:125], v[152:153]
	v_pk_mul_f32 v[162:163], v[120:121], v[118:119]

; template <int MASK> __device__ __forceinline__ float swz_f(float v) { return __builtin_bit_cast(float, __builtin_amdgcn_ds_swizzle(__builtin_bit_cast(int, v), (MASK << 10) | 0x1f)); }
; __device__ __forceinline__ float sum_x32(float v) { const unsigned u = __builtin_bit_cast(unsigned, v); auto rr = __builtin_amdgcn_permlane32_swap(u, u, false, false); return __builtin_bit_cast(float, (unsigned)rr[0]) + __builtin_bit_cast(float, (unsigned)rr[1]); }
;     __device__ __forceinline__ void operator()(const f32x4 (&acc)[2][2][4][2], const Unit& u, int wr, int wc, int fr, int fq) const {
;     ...
;                 if (!GATES && type <= 1) { float ss = 0.f;
; #pragma unroll
;                     for (int bj = 0; bj < 2; ++bj)
; #pragma unroll
;                         for (int n = 0; n < 2; ++n) ss += (v[bj][n][0] * v[bj][n][0] + v[bj][n][1] * v[bj][n][1]) + (v[bj][n][2] * v[bj][n][2] + v[bj][n][3] * v[bj][n][3]);
;                     ss += swz_f<16>(ss); ss = sum_x32(ss);
;                     const float r = __builtin_amdgcn_rsqf(ss * (1.f / 64.f) + EPS) * gsc;
; #pragma unroll
;                     for (int bj = 0; bj < 2; ++bj)
; #pragma unroll
;                         for (int n = 0; n < 2; ++n) v[bj][n] = v[bj][n] * r * *(const f32x4*)(gp + 32 * bj + 4 * n);
.LBB0_278:
	s_and_b64 vcc, exec, s[28:29]
	s_cbranch_vccz .LBB0_280
	v_pk_mul_f32 v[108:109], v[120:121], v[120:121]
	v_pk_mul_f32 v[110:111], v[122:123], v[122:123]
	s_nop 0
	v_pk_mov_b32 v[116:117], v[110:111], v[108:109] op_sel:[1,0]
	v_mov_b32_e32 v111, v109
	v_pk_add_f32 v[108:109], v[116:117], v[110:111]
	v_pk_mul_f32 v[110:111], v[106:107], v[106:107]
	v_pk_add_f32 v[108:109], v[108:109], v[108:109] op_sel_hi:[0,1]
	v_pk_mul_f32 v[116:117], v[104:105], v[104:105]
	v_mul_f32_e32 v108, v100, v100
	v_pk_mov_b32 v[118:119], v[116:117], v[110:111] op_sel:[1,0]
	v_mov_b32_e32 v117, v111
	v_pk_add_f32 v[110:111], v[118:119], v[116:117]
	v_pk_fma_f32 v[116:117], v[100:101], v[100:101], v[108:109] op_sel_hi:[1,1,0]
	v_mul_f32_e32 v108, v102, v102
	v_pk_add_f32 v[110:111], v[110:111], v[110:111] op_sel_hi:[0,1]
	v_pk_fma_f32 v[118:119], v[102:103], v[102:103], v[108:109] op_sel_hi:[1,1,0]
	v_mul_f32_e32 v116, v96, v96
	v_mul_f32_e32 v118, v97, v97
	v_mul_f32_e32 v108, v98, v98
	v_mul_f32_e32 v110, v99, v99
	v_pk_add_f32 v[116:117], v[116:117], v[118:119]
	v_pk_add_f32 v[108:109], v[108:109], v[110:111]
	s_nop 0
	v_pk_add_f32 v[108:109], v[116:117], v[108:109]
	s_nop 0
	v_add_f32_e32 v108, v108, v109
	ds_swizzle_b32 v109, v108 offset:swizzle(SWAP,16)
	s_waitcnt lgkmcnt(0)
	v_add_f32_e32 v108, v108, v109
	v_mov_b32_e32 v109, v108
	s_nop 1
	v_permlane32_swap_b32_e32 v108, v109
	v_add_f32_e32 v108, v108, v109
	v_fmamk_f32 v108, v108, 0x3c800000, v230
	v_rsq_f32_e32 v108, v108
	s_nop 0
	v_mul_f32_e32 v142, v129, v108
	v_pk_mul_f32 v[110:111], v[122:123], v[142:143] op_sel_hi:[1,0]
	v_pk_mul_f32 v[108:109], v[120:121], v[142:143] op_sel_hi:[1,0]
	v_mov_b32_e32 v116, v198
	v_mov_b32_e32 v117, v199
	v_mov_b32_e32 v118, v200
	v_mov_b32_e32 v119, v201
	v_mov_b32_e32 v120, v194
	v_mov_b32_e32 v121, v195
	v_mov_b32_e32 v122, v196
	v_mov_b32_e32 v123, v197
	v_pk_mul_f32 v[104:105], v[104:105], v[142:143] op_sel_hi:[1,0]
	v_pk_mul_f32 v[106:107], v[106:107], v[142:143] op_sel_hi:[1,0]
	v_pk_mul_f32 v[96:97], v[96:97], v[142:143] op_sel_hi:[1,0]
	v_pk_mul_f32 v[98:99], v[98:99], v[142:143] op_sel_hi:[1,0]
	s_nop 0
	v_pk_mul_f32 v[118:119], v[118:119], v[106:107]
	s_nop 0
	v_pk_mul_f32 v[108:109], v[122:123], v[108:109]
	v_pk_mul_f32 v[110:111], v[120:121], v[110:111]
	v_pk_mul_f32 v[116:117], v[116:117], v[104:105]
	v_pk_mul_f32 v[120:121], v[100:101], v[142:143] op_sel_hi:[1,0]
	v_pk_mul_f32 v[122:123], v[102:103], v[142:143] op_sel_hi:[1,0]
	v_mov_b32_e32 v100, v206
	v_mov_b32_e32 v101, v207
	v_mov_b32_e32 v102, v208
	v_mov_b32_e32 v103, v209
	v_mov_b32_e32 v104, v202
	v_mov_b32_e32 v105, v203
	v_mov_b32_e32 v106, v204
	v_mov_b32_e32 v107, v205
	s_nop 0
	v_pk_mul_f32 v[142:143], v[102:103], v[98:99]
	s_nop 0
	v_pk_mul_f32 v[124:125], v[106:107], v[122:123]
	v_pk_mul_f32 v[126:127], v[104:105], v[120:121]
	v_pk_mul_f32 v[144:145], v[100:101], v[96:97]

; template <int MASK> __device__ __forceinline__ float swz_f(float v) { return __builtin_bit_cast(float, __builtin_amdgcn_ds_swizzle(__builtin_bit_cast(int, v), (MASK << 10) | 0x1f)); }
; __device__ __forceinline__ float sum_x32(float v) { const unsigned u = __builtin_bit_cast(unsigned, v); auto rr = __builtin_amdgcn_permlane32_swap(u, u, false, false); return __builtin_bit_cast(float, (unsigned)rr[0]) + __builtin_bit_cast(float, (unsigned)rr[1]); }
;     __device__ __forceinline__ void operator()(const f32x4 (&acc)[2][2][4][2], const Unit& u, int wr, int wc, int fr, int fq) const {
;     ...
;                 if (!GATES && type <= 1) { float ss = 0.f;
; #pragma unroll
;                     for (int bj = 0; bj < 2; ++bj)
; #pragma unroll
;                         for (int n = 0; n < 2; ++n) ss += (v[bj][n][0] * v[bj][n][0] + v[bj][n][1] * v[bj][n][1]) + (v[bj][n][2] * v[bj][n][2] + v[bj][n][3] * v[bj][n][3]);
;                     ss += swz_f<16>(ss); ss = sum_x32(ss);
;                     const float r = __builtin_amdgcn_rsqf(ss * (1.f / 64.f) + EPS) * gsc;
; #pragma unroll
;                     for (int bj = 0; bj < 2; ++bj)
; #pragma unroll
;                         for (int n = 0; n < 2; ++n) v[bj][n] = v[bj][n] * r * *(const f32x4*)(gp + 32 * bj + 4 * n);
.LBB0_287:
	s_and_b64 vcc, exec, s[28:29]
	s_cbranch_vccz .LBB0_289
	v_pk_mul_f32 v[92:93], v[100:101], v[100:101]
	v_pk_mul_f32 v[94:95], v[102:103], v[102:103]
	s_nop 0
	v_pk_mov_b32 v[96:97], v[94:95], v[92:93] op_sel:[1,0]
	v_mov_b32_e32 v95, v93
	v_pk_add_f32 v[92:93], v[96:97], v[94:95]
	v_pk_mul_f32 v[94:95], v[90:91], v[90:91]
	v_pk_add_f32 v[92:93], v[92:93], v[92:93] op_sel_hi:[0,1]
	v_pk_mul_f32 v[96:97], v[88:89], v[88:89]
	v_mul_f32_e32 v92, v84, v84
	v_pk_mov_b32 v[98:99], v[96:97], v[94:95] op_sel:[1,0]
	v_mov_b32_e32 v97, v95
	v_pk_add_f32 v[94:95], v[98:99], v[96:97]
	v_pk_fma_f32 v[96:97], v[84:85], v[84:85], v[92:93] op_sel_hi:[1,1,0]
	v_mul_f32_e32 v92, v86, v86
	v_pk_add_f32 v[94:95], v[94:95], v[94:95] op_sel_hi:[0,1]
	v_pk_fma_f32 v[98:99], v[86:87], v[86:87], v[92:93] op_sel_hi:[1,1,0]
	v_mul_f32_e32 v96, v80, v80
	v_mul_f32_e32 v98, v81, v81
	v_mul_f32_e32 v92, v82, v82
	v_mul_f32_e32 v94, v83, v83
	v_pk_add_f32 v[96:97], v[96:97], v[98:99]
	v_pk_add_f32 v[92:93], v[92:93], v[94:95]
	s_nop 0
	v_pk_add_f32 v[92:93], v[96:97], v[92:93]
	s_nop 0
	v_add_f32_e32 v92, v92, v93
	ds_swizzle_b32 v93, v92 offset:swizzle(SWAP,16)
	s_waitcnt lgkmcnt(0)
	v_add_f32_e32 v92, v92, v93
	v_mov_b32_e32 v93, v92
	s_nop 1
	v_permlane32_swap_b32_e32 v92, v93
	v_add_f32_e32 v92, v92, v93
	v_fmamk_f32 v92, v92, 0x3c800000, v230
	v_rsq_f32_e32 v92, v92
	s_nop 0
	v_mul_f32_e32 v108, v129, v92
	v_pk_mul_f32 v[94:95], v[102:103], v[108:109] op_sel_hi:[1,0]
	v_pk_mul_f32 v[92:93], v[100:101], v[108:109] op_sel_hi:[1,0]
	v_mov_b32_e32 v96, v198
	v_mov_b32_e32 v97, v199
	v_mov_b32_e32 v98, v200
	v_mov_b32_e32 v99, v201
	v_mov_b32_e32 v100, v194
	v_mov_b32_e32 v101, v195
	v_mov_b32_e32 v102, v196
	v_mov_b32_e32 v103, v197
	v_pk_mul_f32 v[88:89], v[88:89], v[108:109] op_sel_hi:[1,0]
	v_pk_mul_f32 v[90:91], v[90:91], v[108:109] op_sel_hi:[1,0]
	v_pk_mul_f32 v[80:81], v[80:81], v[108:109] op_sel_hi:[1,0]
	v_pk_mul_f32 v[82:83], v[82:83], v[108:109] op_sel_hi:[1,0]
	s_nop 0
	v_pk_mul_f32 v[98:99], v[98:99], v[90:91]
	s_nop 0
	v_pk_mul_f32 v[92:93], v[102:103], v[92:93]
	v_pk_mul_f32 v[94:95], v[100:101], v[94:95]
	v_pk_mul_f32 v[96:97], v[96:97], v[88:89]
	v_pk_mul_f32 v[100:101], v[84:85], v[108:109] op_sel_hi:[1,0]
	v_pk_mul_f32 v[102:103], v[86:87], v[108:109] op_sel_hi:[1,0]
	v_mov_b32_e32 v84, v206
	v_mov_b32_e32 v85, v207
	v_mov_b32_e32 v86, v208
	v_mov_b32_e32 v87, v209
	v_mov_b32_e32 v88, v202
	v_mov_b32_e32 v89, v203
	v_mov_b32_e32 v90, v204
	v_mov_b32_e32 v91, v205
	s_nop 0
	v_pk_mul_f32 v[108:109], v[86:87], v[82:83]
	s_nop 0
	v_pk_mul_f32 v[104:105], v[90:91], v[102:103]
	v_pk_mul_f32 v[106:107], v[88:89], v[100:101]
	v_pk_mul_f32 v[110:111], v[84:85], v[80:81]

; template <int MASK> __device__ __forceinline__ float swz_f(float v) { return __builtin_bit_cast(float, __builtin_amdgcn_ds_swizzle(__builtin_bit_cast(int, v), (MASK << 10) | 0x1f)); }
; __device__ __forceinline__ float sum_x32(float v) { const unsigned u = __builtin_bit_cast(unsigned, v); auto rr = __builtin_amdgcn_permlane32_swap(u, u, false, false); return __builtin_bit_cast(float, (unsigned)rr[0]) + __builtin_bit_cast(float, (unsigned)rr[1]); }
;     __device__ __forceinline__ void operator()(const f32x4 (&acc)[2][2][4][2], const Unit& u, int wr, int wc, int fr, int fq) const {
;     ...
;                 if (!GATES && type <= 1) { float ss = 0.f;
; #pragma unroll
;                     for (int bj = 0; bj < 2; ++bj)
; #pragma unroll
;                         for (int n = 0; n < 2; ++n) ss += (v[bj][n][0] * v[bj][n][0] + v[bj][n][1] * v[bj][n][1]) + (v[bj][n][2] * v[bj][n][2] + v[bj][n][3] * v[bj][n][3]);
;                     ss += swz_f<16>(ss); ss = sum_x32(ss);
;                     const float r = __builtin_amdgcn_rsqf(ss * (1.f / 64.f) + EPS) * gsc;
; #pragma unroll
;                     for (int bj = 0; bj < 2; ++bj)
; #pragma unroll
;                         for (int n = 0; n < 2; ++n) v[bj][n] = v[bj][n] * r * *(const f32x4*)(gp + 32 * bj + 4 * n);
.LBB0_296:
	s_and_b64 vcc, exec, s[28:29]
	s_cbranch_vccz .LBB0_298
	v_pk_mul_f32 v[76:77], v[84:85], v[84:85]
	v_pk_mul_f32 v[78:79], v[86:87], v[86:87]
	s_nop 0
	v_pk_mov_b32 v[80:81], v[78:79], v[76:77] op_sel:[1,0]
	v_mov_b32_e32 v79, v77
	v_pk_add_f32 v[76:77], v[80:81], v[78:79]
	v_pk_mul_f32 v[78:79], v[74:75], v[74:75]
	v_pk_add_f32 v[76:77], v[76:77], v[76:77] op_sel_hi:[0,1]
	v_pk_mul_f32 v[80:81], v[72:73], v[72:73]
	v_mul_f32_e32 v76, v68, v68
	v_pk_mov_b32 v[82:83], v[80:81], v[78:79] op_sel:[1,0]
	v_mov_b32_e32 v81, v79
	v_pk_add_f32 v[78:79], v[82:83], v[80:81]
	v_pk_fma_f32 v[80:81], v[68:69], v[68:69], v[76:77] op_sel_hi:[1,1,0]
	v_mul_f32_e32 v76, v70, v70
	v_pk_add_f32 v[78:79], v[78:79], v[78:79] op_sel_hi:[0,1]
	v_pk_fma_f32 v[82:83], v[70:71], v[70:71], v[76:77] op_sel_hi:[1,1,0]
	v_mul_f32_e32 v80, v64, v64
	v_mul_f32_e32 v82, v65, v65
	v_mul_f32_e32 v76, v66, v66
	v_mul_f32_e32 v78, v67, v67
	v_pk_add_f32 v[80:81], v[80:81], v[82:83]
	v_pk_add_f32 v[76:77], v[76:77], v[78:79]
	s_nop 0
	v_pk_add_f32 v[76:77], v[80:81], v[76:77]
	s_nop 0
	v_add_f32_e32 v76, v76, v77
	ds_swizzle_b32 v77, v76 offset:swizzle(SWAP,16)
	s_waitcnt lgkmcnt(0)
	v_add_f32_e32 v76, v76, v77
	v_mov_b32_e32 v77, v76
	s_nop 1
	v_permlane32_swap_b32_e32 v76, v77
	v_add_f32_e32 v76, v76, v77
	v_fmamk_f32 v76, v76, 0x3c800000, v230
	v_rsq_f32_e32 v76, v76
	s_nop 0
	v_mul_f32_e32 v92, v129, v76
	v_pk_mul_f32 v[78:79], v[86:87], v[92:93] op_sel_hi:[1,0]
	v_pk_mul_f32 v[76:77], v[84:85], v[92:93] op_sel_hi:[1,0]
	v_mov_b32_e32 v80, v198
	v_mov_b32_e32 v81, v199
	v_mov_b32_e32 v82, v200
	v_mov_b32_e32 v83, v201
	v_mov_b32_e32 v84, v194
	v_mov_b32_e32 v85, v195
	v_mov_b32_e32 v86, v196
	v_mov_b32_e32 v87, v197
	v_pk_mul_f32 v[72:73], v[72:73], v[92:93] op_sel_hi:[1,0]
	v_pk_mul_f32 v[74:75], v[74:75], v[92:93] op_sel_hi:[1,0]
	v_pk_mul_f32 v[64:65], v[64:65], v[92:93] op_sel_hi:[1,0]
	v_pk_mul_f32 v[66:67], v[66:67], v[92:93] op_sel_hi:[1,0]
	s_nop 0
	v_pk_mul_f32 v[82:83], v[82:83], v[74:75]
	s_nop 0
	v_pk_mul_f32 v[76:77], v[86:87], v[76:77]
	v_pk_mul_f32 v[78:79], v[84:85], v[78:79]
	v_pk_mul_f32 v[80:81], v[80:81], v[72:73]
	v_pk_mul_f32 v[84:85], v[68:69], v[92:93] op_sel_hi:[1,0]
	v_pk_mul_f32 v[86:87], v[70:71], v[92:93] op_sel_hi:[1,0]
	v_mov_b32_e32 v68, v206
	v_mov_b32_e32 v69, v207
	v_mov_b32_e32 v70, v208
	v_mov_b32_e32 v71, v209
	v_mov_b32_e32 v72, v202
	v_mov_b32_e32 v73, v203
	v_mov_b32_e32 v74, v204
	v_mov_b32_e32 v75, v205
	s_nop 0
	v_pk_mul_f32 v[92:93], v[70:71], v[66:67]
	s_nop 0
	v_pk_mul_f32 v[88:89], v[74:75], v[86:87]
	v_pk_mul_f32 v[90:91], v[72:73], v[84:85]
	v_pk_mul_f32 v[94:95], v[68:69], v[64:65]

; template <int MASK> __device__ __forceinline__ float swz_f(float v) { return __builtin_bit_cast(float, __builtin_amdgcn_ds_swizzle(__builtin_bit_cast(int, v), (MASK << 10) | 0x1f)); }
; __device__ __forceinline__ float sum_x32(float v) { const unsigned u = __builtin_bit_cast(unsigned, v); auto rr = __builtin_amdgcn_permlane32_swap(u, u, false, false); return __builtin_bit_cast(float, (unsigned)rr[0]) + __builtin_bit_cast(float, (unsigned)rr[1]); }
;     __device__ __forceinline__ void operator()(const f32x4 (&acc)[2][2][4][2], const Unit& u, int wr, int wc, int fr, int fq) const {
;     ...
;                 if (!GATES && type <= 1) { float ss = 0.f;
; #pragma unroll
;                     for (int bj = 0; bj < 2; ++bj)
; #pragma unroll
;                         for (int n = 0; n < 2; ++n) ss += (v[bj][n][0] * v[bj][n][0] + v[bj][n][1] * v[bj][n][1]) + (v[bj][n][2] * v[bj][n][2] + v[bj][n][3] * v[bj][n][3]);
;                     ss += swz_f<16>(ss); ss = sum_x32(ss);
;                     const float r = __builtin_amdgcn_rsqf(ss * (1.f / 64.f) + EPS) * gsc;
; #pragma unroll
;                     for (int bj = 0; bj < 2; ++bj)
; #pragma unroll
;                         for (int n = 0; n < 2; ++n) v[bj][n] = v[bj][n] * r * *(const f32x4*)(gp + 32 * bj + 4 * n);
.LBB0_305:
	s_and_b64 vcc, exec, s[28:29]
	s_cbranch_vccz .LBB0_307
	v_pk_mul_f32 v[60:61], v[68:69], v[68:69]
	v_pk_mul_f32 v[62:63], v[70:71], v[70:71]
	s_nop 0
	v_pk_mov_b32 v[64:65], v[62:63], v[60:61] op_sel:[1,0]
	v_mov_b32_e32 v63, v61
	v_pk_add_f32 v[60:61], v[64:65], v[62:63]
	v_pk_mul_f32 v[62:63], v[58:59], v[58:59]
	v_pk_add_f32 v[60:61], v[60:61], v[60:61] op_sel_hi:[0,1]
	v_pk_mul_f32 v[64:65], v[56:57], v[56:57]
	v_mul_f32_e32 v60, v52, v52
	v_pk_mov_b32 v[66:67], v[64:65], v[62:63] op_sel:[1,0]
	v_mov_b32_e32 v65, v63
	v_pk_add_f32 v[62:63], v[66:67], v[64:65]
	v_pk_fma_f32 v[64:65], v[52:53], v[52:53], v[60:61] op_sel_hi:[1,1,0]
	v_mul_f32_e32 v60, v54, v54
	v_pk_add_f32 v[62:63], v[62:63], v[62:63] op_sel_hi:[0,1]
	v_pk_fma_f32 v[66:67], v[54:55], v[54:55], v[60:61] op_sel_hi:[1,1,0]
	v_mul_f32_e32 v64, v48, v48
	v_mul_f32_e32 v66, v49, v49
	v_mul_f32_e32 v60, v50, v50
	v_mul_f32_e32 v62, v51, v51
	v_pk_add_f32 v[64:65], v[64:65], v[66:67]
	v_pk_add_f32 v[60:61], v[60:61], v[62:63]
	s_nop 0
	v_pk_add_f32 v[60:61], v[64:65], v[60:61]
	s_nop 0
	v_add_f32_e32 v60, v60, v61
	ds_swizzle_b32 v61, v60 offset:swizzle(SWAP,16)
	s_waitcnt lgkmcnt(0)
	v_add_f32_e32 v60, v60, v61
	v_mov_b32_e32 v61, v60
	s_nop 1
	v_permlane32_swap_b32_e32 v60, v61
	v_add_f32_e32 v60, v60, v61
	v_fmamk_f32 v60, v60, 0x3c800000, v230
	v_rsq_f32_e32 v60, v60
	s_nop 0
	v_mul_f32_e32 v76, v129, v60
	v_pk_mul_f32 v[62:63], v[70:71], v[76:77] op_sel_hi:[1,0]
	v_pk_mul_f32 v[60:61], v[68:69], v[76:77] op_sel_hi:[1,0]
	v_mov_b32_e32 v64, v198
	v_mov_b32_e32 v65, v199
	v_mov_b32_e32 v66, v200
	v_mov_b32_e32 v67, v201
	v_mov_b32_e32 v68, v194
	v_mov_b32_e32 v69, v195
	v_mov_b32_e32 v70, v196
	v_mov_b32_e32 v71, v197
	v_pk_mul_f32 v[56:57], v[56:57], v[76:77] op_sel_hi:[1,0]
	v_pk_mul_f32 v[58:59], v[58:59], v[76:77] op_sel_hi:[1,0]
	v_pk_mul_f32 v[48:49], v[48:49], v[76:77] op_sel_hi:[1,0]
	v_pk_mul_f32 v[50:51], v[50:51], v[76:77] op_sel_hi:[1,0]
	s_nop 0
	v_pk_mul_f32 v[66:67], v[66:67], v[58:59]
	s_nop 0
	v_pk_mul_f32 v[60:61], v[70:71], v[60:61]
	v_pk_mul_f32 v[62:63], v[68:69], v[62:63]
	v_pk_mul_f32 v[64:65], v[64:65], v[56:57]
	v_pk_mul_f32 v[68:69], v[52:53], v[76:77] op_sel_hi:[1,0]
	v_pk_mul_f32 v[70:71], v[54:55], v[76:77] op_sel_hi:[1,0]
	v_mov_b32_e32 v52, v206
	v_mov_b32_e32 v53, v207
	v_mov_b32_e32 v54, v208
	v_mov_b32_e32 v55, v209
	v_mov_b32_e32 v56, v202
	v_mov_b32_e32 v57, v203
	v_mov_b32_e32 v58, v204
	v_mov_b32_e32 v59, v205
	s_nop 0
	v_pk_mul_f32 v[76:77], v[54:55], v[50:51]
	s_nop 0
	v_pk_mul_f32 v[72:73], v[58:59], v[70:71]
	v_pk_mul_f32 v[74:75], v[56:57], v[68:69]
	v_pk_mul_f32 v[78:79], v[52:53], v[48:49]

; template <int MASK> __device__ __forceinline__ float swz_f(float v) { return __builtin_bit_cast(float, __builtin_amdgcn_ds_swizzle(__builtin_bit_cast(int, v), (MASK << 10) | 0x1f)); }
; __device__ __forceinline__ float sum_x32(float v) { const unsigned u = __builtin_bit_cast(unsigned, v); auto rr = __builtin_amdgcn_permlane32_swap(u, u, false, false); return __builtin_bit_cast(float, (unsigned)rr[0]) + __builtin_bit_cast(float, (unsigned)rr[1]); }
;     __device__ __forceinline__ void operator()(const f32x4 (&acc)[2][2][4][2], const Unit& u, int wr, int wc, int fr, int fq) const {
;     ...
;                 if (!GATES && type <= 1) { float ss = 0.f;
; #pragma unroll
;                     for (int bj = 0; bj < 2; ++bj)
; #pragma unroll
;                         for (int n = 0; n < 2; ++n) ss += (v[bj][n][0] * v[bj][n][0] + v[bj][n][1] * v[bj][n][1]) + (v[bj][n][2] * v[bj][n][2] + v[bj][n][3] * v[bj][n][3]);
;                     ss += swz_f<16>(ss); ss = sum_x32(ss);
;                     const float r = __builtin_amdgcn_rsqf(ss * (1.f / 64.f) + EPS) * gsc;
; #pragma unroll
;                     for (int bj = 0; bj < 2; ++bj)
; #pragma unroll
;                         for (int n = 0; n < 2; ++n) v[bj][n] = v[bj][n] * r * *(const f32x4*)(gp + 32 * bj + 4 * n);
.LBB0_314:
	s_and_b64 vcc, exec, s[28:29]
	s_cbranch_vccz .LBB0_316
	v_pk_mul_f32 v[44:45], v[52:53], v[52:53]
	v_pk_mul_f32 v[46:47], v[54:55], v[54:55]
	s_nop 0
	v_pk_mov_b32 v[48:49], v[46:47], v[44:45] op_sel:[1,0]
	v_mov_b32_e32 v47, v45
	v_pk_add_f32 v[44:45], v[48:49], v[46:47]
	v_pk_mul_f32 v[46:47], v[42:43], v[42:43]
	v_pk_add_f32 v[44:45], v[44:45], v[44:45] op_sel_hi:[0,1]
	v_pk_mul_f32 v[48:49], v[40:41], v[40:41]
	v_mul_f32_e32 v44, v36, v36
	v_pk_mov_b32 v[50:51], v[48:49], v[46:47] op_sel:[1,0]
	v_mov_b32_e32 v49, v47
	v_pk_add_f32 v[46:47], v[50:51], v[48:49]
	v_pk_fma_f32 v[48:49], v[36:37], v[36:37], v[44:45] op_sel_hi:[1,1,0]
	v_mul_f32_e32 v44, v38, v38
	v_pk_add_f32 v[46:47], v[46:47], v[46:47] op_sel_hi:[0,1]
	v_pk_fma_f32 v[50:51], v[38:39], v[38:39], v[44:45] op_sel_hi:[1,1,0]
	v_mul_f32_e32 v48, v32, v32
	v_mul_f32_e32 v50, v33, v33
	v_mul_f32_e32 v44, v34, v34
	v_mul_f32_e32 v46, v35, v35
	v_pk_add_f32 v[48:49], v[48:49], v[50:51]
	v_pk_add_f32 v[44:45], v[44:45], v[46:47]
	s_nop 0
	v_pk_add_f32 v[44:45], v[48:49], v[44:45]
	s_nop 0
	v_add_f32_e32 v44, v44, v45
	ds_swizzle_b32 v45, v44 offset:swizzle(SWAP,16)
	s_waitcnt lgkmcnt(0)
	v_add_f32_e32 v44, v44, v45
	v_mov_b32_e32 v45, v44
	s_nop 1
	v_permlane32_swap_b32_e32 v44, v45
	v_add_f32_e32 v44, v44, v45
	v_fmamk_f32 v44, v44, 0x3c800000, v230
	v_rsq_f32_e32 v44, v44
	s_nop 0
	v_mul_f32_e32 v60, v129, v44
	v_pk_mul_f32 v[46:47], v[54:55], v[60:61] op_sel_hi:[1,0]
	v_pk_mul_f32 v[44:45], v[52:53], v[60:61] op_sel_hi:[1,0]
	v_mov_b32_e32 v48, v198
	v_mov_b32_e32 v49, v199
	v_mov_b32_e32 v50, v200
	v_mov_b32_e32 v51, v201
	v_mov_b32_e32 v52, v194
	v_mov_b32_e32 v53, v195
	v_mov_b32_e32 v54, v196
	v_mov_b32_e32 v55, v197
	v_pk_mul_f32 v[40:41], v[40:41], v[60:61] op_sel_hi:[1,0]
	v_pk_mul_f32 v[42:43], v[42:43], v[60:61] op_sel_hi:[1,0]
	v_pk_mul_f32 v[32:33], v[32:33], v[60:61] op_sel_hi:[1,0]
	v_pk_mul_f32 v[34:35], v[34:35], v[60:61] op_sel_hi:[1,0]
	s_nop 0
	v_pk_mul_f32 v[50:51], v[50:51], v[42:43]
	s_nop 0
	v_pk_mul_f32 v[44:45], v[54:55], v[44:45]
	v_pk_mul_f32 v[46:47], v[52:53], v[46:47]
	v_pk_mul_f32 v[48:49], v[48:49], v[40:41]
	v_pk_mul_f32 v[52:53], v[36:37], v[60:61] op_sel_hi:[1,0]
	v_pk_mul_f32 v[54:55], v[38:39], v[60:61] op_sel_hi:[1,0]
	v_mov_b32_e32 v36, v206
	v_mov_b32_e32 v37, v207
	v_mov_b32_e32 v38, v208
	v_mov_b32_e32 v39, v209
	v_mov_b32_e32 v40, v202
	v_mov_b32_e32 v41, v203
	v_mov_b32_e32 v42, v204
	v_mov_b32_e32 v43, v205
	s_nop 0
	v_pk_mul_f32 v[60:61], v[38:39], v[34:35]
	s_nop 0
	v_pk_mul_f32 v[56:57], v[42:43], v[54:55]
	v_pk_mul_f32 v[58:59], v[40:41], v[52:53]
	v_pk_mul_f32 v[62:63], v[36:37], v[32:33]

; template <int MASK> __device__ __forceinline__ float swz_f(float v) { return __builtin_bit_cast(float, __builtin_amdgcn_ds_swizzle(__builtin_bit_cast(int, v), (MASK << 10) | 0x1f)); }
; __device__ __forceinline__ float sum_x32(float v) { const unsigned u = __builtin_bit_cast(unsigned, v); auto rr = __builtin_amdgcn_permlane32_swap(u, u, false, false); return __builtin_bit_cast(float, (unsigned)rr[0]) + __builtin_bit_cast(float, (unsigned)rr[1]); }
;     __device__ __forceinline__ void operator()(const f32x4 (&acc)[2][2][4][2], const Unit& u, int wr, int wc, int fr, int fq) const {
;     ...
;                 if (!GATES && type <= 1) { float ss = 0.f;
; #pragma unroll
;                     for (int bj = 0; bj < 2; ++bj)
; #pragma unroll
;                         for (int n = 0; n < 2; ++n) ss += (v[bj][n][0] * v[bj][n][0] + v[bj][n][1] * v[bj][n][1]) + (v[bj][n][2] * v[bj][n][2] + v[bj][n][3] * v[bj][n][3]);
;                     ss += swz_f<16>(ss); ss = sum_x32(ss);
;                     const float r = __builtin_amdgcn_rsqf(ss * (1.f / 64.f) + EPS) * gsc;
; #pragma unroll
;                     for (int bj = 0; bj < 2; ++bj)
; #pragma unroll
;                         for (int n = 0; n < 2; ++n) v[bj][n] = v[bj][n] * r * *(const f32x4*)(gp + 32 * bj + 4 * n);
.LBB0_323:
	s_and_b64 vcc, exec, s[28:29]
	s_cbranch_vccz .LBB0_325
	v_pk_mul_f32 v[28:29], v[36:37], v[36:37]
	v_pk_mul_f32 v[30:31], v[38:39], v[38:39]
	s_nop 0
	v_pk_mov_b32 v[32:33], v[30:31], v[28:29] op_sel:[1,0]
	v_mov_b32_e32 v31, v29
	v_pk_add_f32 v[28:29], v[32:33], v[30:31]
	v_pk_mul_f32 v[30:31], v[26:27], v[26:27]
	v_pk_add_f32 v[28:29], v[28:29], v[28:29] op_sel_hi:[0,1]
	v_pk_mul_f32 v[32:33], v[24:25], v[24:25]
	v_mul_f32_e32 v28, v20, v20
	v_pk_mov_b32 v[34:35], v[32:33], v[30:31] op_sel:[1,0]
	v_mov_b32_e32 v33, v31
	v_pk_add_f32 v[30:31], v[34:35], v[32:33]
	v_pk_fma_f32 v[32:33], v[20:21], v[20:21], v[28:29] op_sel_hi:[1,1,0]
	v_mul_f32_e32 v28, v22, v22
	v_pk_add_f32 v[30:31], v[30:31], v[30:31] op_sel_hi:[0,1]
	v_pk_fma_f32 v[34:35], v[22:23], v[22:23], v[28:29] op_sel_hi:[1,1,0]
	v_mul_f32_e32 v32, v16, v16
	v_mul_f32_e32 v34, v17, v17
	v_mul_f32_e32 v28, v18, v18
	v_mul_f32_e32 v30, v19, v19
	v_pk_add_f32 v[32:33], v[32:33], v[34:35]
	v_pk_add_f32 v[28:29], v[28:29], v[30:31]
	s_nop 0
	v_pk_add_f32 v[28:29], v[32:33], v[28:29]
	s_nop 0
	v_add_f32_e32 v28, v28, v29
	ds_swizzle_b32 v29, v28 offset:swizzle(SWAP,16)
	s_waitcnt lgkmcnt(0)
	v_add_f32_e32 v28, v28, v29
	v_mov_b32_e32 v29, v28
	s_nop 1
	v_permlane32_swap_b32_e32 v28, v29
	v_add_f32_e32 v28, v28, v29
	v_fmamk_f32 v28, v28, 0x3c800000, v230
	v_rsq_f32_e32 v28, v28
	s_nop 0
	v_mul_f32_e32 v44, v129, v28
	v_pk_mul_f32 v[30:31], v[38:39], v[44:45] op_sel_hi:[1,0]
	v_pk_mul_f32 v[28:29], v[36:37], v[44:45] op_sel_hi:[1,0]
	v_mov_b32_e32 v32, v198
	v_mov_b32_e32 v33, v199
	v_mov_b32_e32 v34, v200
	v_mov_b32_e32 v35, v201
	v_mov_b32_e32 v36, v194
	v_mov_b32_e32 v37, v195
	v_mov_b32_e32 v38, v196
	v_mov_b32_e32 v39, v197
	v_pk_mul_f32 v[24:25], v[24:25], v[44:45] op_sel_hi:[1,0]
	v_pk_mul_f32 v[26:27], v[26:27], v[44:45] op_sel_hi:[1,0]
	v_pk_mul_f32 v[16:17], v[16:17], v[44:45] op_sel_hi:[1,0]
	v_pk_mul_f32 v[18:19], v[18:19], v[44:45] op_sel_hi:[1,0]
	s_nop 0
	v_pk_mul_f32 v[34:35], v[34:35], v[26:27]
	s_nop 0
	v_pk_mul_f32 v[28:29], v[38:39], v[28:29]
	v_pk_mul_f32 v[30:31], v[36:37], v[30:31]
	v_pk_mul_f32 v[32:33], v[32:33], v[24:25]
	v_pk_mul_f32 v[36:37], v[20:21], v[44:45] op_sel_hi:[1,0]
	v_pk_mul_f32 v[38:39], v[22:23], v[44:45] op_sel_hi:[1,0]
	v_mov_b32_e32 v20, v206
	v_mov_b32_e32 v21, v207
	v_mov_b32_e32 v22, v208
	v_mov_b32_e32 v23, v209
	v_mov_b32_e32 v24, v202
	v_mov_b32_e32 v25, v203
	v_mov_b32_e32 v26, v204
	v_mov_b32_e32 v27, v205
	s_nop 0
	v_pk_mul_f32 v[44:45], v[22:23], v[18:19]
	s_nop 0
	v_pk_mul_f32 v[40:41], v[26:27], v[38:39]
	v_pk_mul_f32 v[42:43], v[24:25], v[36:37]
	v_pk_mul_f32 v[46:47], v[20:21], v[16:17]

; template <int MASK> __device__ __forceinline__ float swz_f(float v) { return __builtin_bit_cast(float, __builtin_amdgcn_ds_swizzle(__builtin_bit_cast(int, v), (MASK << 10) | 0x1f)); }
; __device__ __forceinline__ float sum_x32(float v) { const unsigned u = __builtin_bit_cast(unsigned, v); auto rr = __builtin_amdgcn_permlane32_swap(u, u, false, false); return __builtin_bit_cast(float, (unsigned)rr[0]) + __builtin_bit_cast(float, (unsigned)rr[1]); }
;     __device__ __forceinline__ void operator()(const f32x4 (&acc)[2][2][4][2], const Unit& u, int wr, int wc, int fr, int fq) const {
;     ...
;                 if (!GATES && type <= 1) { float ss = 0.f;
; #pragma unroll
;                     for (int bj = 0; bj < 2; ++bj)
; #pragma unroll
;                         for (int n = 0; n < 2; ++n) ss += (v[bj][n][0] * v[bj][n][0] + v[bj][n][1] * v[bj][n][1]) + (v[bj][n][2] * v[bj][n][2] + v[bj][n][3] * v[bj][n][3]);
;                     ss += swz_f<16>(ss); ss = sum_x32(ss);
;                     const float r = __builtin_amdgcn_rsqf(ss * (1.f / 64.f) + EPS) * gsc;
; #pragma unroll
;                     for (int bj = 0; bj < 2; ++bj)
; #pragma unroll
;                         for (int n = 0; n < 2; ++n) v[bj][n] = v[bj][n] * r * *(const f32x4*)(gp + 32 * bj + 4 * n);
.LBB0_332:
	s_and_b64 vcc, exec, s[2:3]
	s_cbranch_vccz .LBB0_334
	v_pk_mul_f32 v[12:13], v[20:21], v[20:21]
	v_pk_mul_f32 v[14:15], v[22:23], v[22:23]
	s_nop 0
	v_pk_mov_b32 v[16:17], v[14:15], v[12:13] op_sel:[1,0]
	v_mov_b32_e32 v15, v13
	v_pk_add_f32 v[12:13], v[16:17], v[14:15]
	v_pk_mul_f32 v[14:15], v[10:11], v[10:11]
	v_pk_add_f32 v[12:13], v[12:13], v[12:13] op_sel_hi:[0,1]
	v_pk_mul_f32 v[16:17], v[8:9], v[8:9]
	v_mul_f32_e32 v12, v4, v4
	v_pk_mov_b32 v[18:19], v[16:17], v[14:15] op_sel:[1,0]
	v_mov_b32_e32 v17, v15
	v_pk_add_f32 v[14:15], v[18:19], v[16:17]
	v_pk_fma_f32 v[16:17], v[4:5], v[4:5], v[12:13] op_sel_hi:[1,1,0]
	v_mul_f32_e32 v12, v6, v6
	v_pk_add_f32 v[14:15], v[14:15], v[14:15] op_sel_hi:[0,1]
	v_pk_fma_f32 v[18:19], v[6:7], v[6:7], v[12:13] op_sel_hi:[1,1,0]
	v_mul_f32_e32 v16, v0, v0
	v_mul_f32_e32 v18, v1, v1
	v_mul_f32_e32 v12, v2, v2
	v_mul_f32_e32 v14, v3, v3
	v_pk_add_f32 v[16:17], v[16:17], v[18:19]
	v_pk_add_f32 v[12:13], v[12:13], v[14:15]
	s_nop 0
	v_pk_add_f32 v[12:13], v[16:17], v[12:13]
	s_nop 0
	v_add_f32_e32 v12, v12, v13
	ds_swizzle_b32 v13, v12 offset:swizzle(SWAP,16)
	s_waitcnt lgkmcnt(0)
	v_add_f32_e32 v12, v12, v13
	v_mov_b32_e32 v13, v12
	s_nop 1
	v_permlane32_swap_b32_e32 v12, v13
	v_add_f32_e32 v12, v12, v13
	v_fmamk_f32 v12, v12, 0x3c800000, v230
	v_rsq_f32_e32 v12, v12
	s_nop 0
	v_mul_f32_e32 v28, v129, v12
	v_pk_mul_f32 v[14:15], v[22:23], v[28:29] op_sel_hi:[1,0]
	v_pk_mul_f32 v[12:13], v[20:21], v[28:29] op_sel_hi:[1,0]
	v_mov_b32_e32 v16, v198
	v_mov_b32_e32 v17, v199
	v_mov_b32_e32 v18, v200
	v_mov_b32_e32 v19, v201
	v_mov_b32_e32 v20, v194
	v_mov_b32_e32 v21, v195
	v_mov_b32_e32 v22, v196
	v_mov_b32_e32 v23, v197
	v_pk_mul_f32 v[8:9], v[8:9], v[28:29] op_sel_hi:[1,0]
	v_pk_mul_f32 v[10:11], v[10:11], v[28:29] op_sel_hi:[1,0]
	v_pk_mul_f32 v[0:1], v[0:1], v[28:29] op_sel_hi:[1,0]
	v_pk_mul_f32 v[2:3], v[2:3], v[28:29] op_sel_hi:[1,0]
	s_nop 0
	v_pk_mul_f32 v[18:19], v[18:19], v[10:11]
	s_nop 0
	v_pk_mul_f32 v[12:13], v[22:23], v[12:13]
	v_pk_mul_f32 v[14:15], v[20:21], v[14:15]
	v_pk_mul_f32 v[16:17], v[16:17], v[8:9]
	v_pk_mul_f32 v[20:21], v[4:5], v[28:29] op_sel_hi:[1,0]
	v_pk_mul_f32 v[22:23], v[6:7], v[28:29] op_sel_hi:[1,0]
	v_mov_b32_e32 v4, v206
	v_mov_b32_e32 v5, v207
	v_mov_b32_e32 v6, v208
	v_mov_b32_e32 v7, v209
	v_mov_b32_e32 v8, v202
	v_mov_b32_e32 v9, v203
	v_mov_b32_e32 v10, v204
	v_mov_b32_e32 v11, v205
	s_nop 0
	v_pk_mul_f32 v[28:29], v[6:7], v[2:3]
	s_nop 0
	v_pk_mul_f32 v[24:25], v[10:11], v[22:23]
	v_pk_mul_f32 v[26:27], v[8:9], v[20:21]
	v_pk_mul_f32 v[30:31], v[4:5], v[0:1]

; template <int MASK> __device__ __forceinline__ float swz_f(float v) { return __builtin_bit_cast(float, __builtin_amdgcn_ds_swizzle(__builtin_bit_cast(int, v), (MASK << 10) | 0x1f)); }
; __device__ __forceinline__ float sum_x32(float v) { const unsigned u = __builtin_bit_cast(unsigned, v); auto rr = __builtin_amdgcn_permlane32_swap(u, u, false, false); return __builtin_bit_cast(float, (unsigned)rr[0]) + __builtin_bit_cast(float, (unsigned)rr[1]); }
; __device__ __forceinline__ u32x4 pack8(const f32x4 a, const f32x4 b) { u32x4 w; w.x = cvt_pk_bf16(a[0], a[1]); w.y = cvt_pk_bf16(a[2], a[3]); w.z = cvt_pk_bf16(b[0], b[1]); w.w = cvt_pk_bf16(b[2], b[3]); return w; }
;     __device__ __forceinline__ void operator()(const f32x4 (&acc)[2][2][4][2], const Unit& u, int wr, int wc, int fr, int fq) const {
;     ...
;                 if (!GATES && type <= 1) { float ss = 0.f;
; #pragma unroll
;                     for (int bj = 0; bj < 2; ++bj)
; #pragma unroll
;                         for (int n = 0; n < 2; ++n) ss += (v[bj][n][0] * v[bj][n][0] + v[bj][n][1] * v[bj][n][1]) + (v[bj][n][2] * v[bj][n][2] + v[bj][n][3] * v[bj][n][3]);
;                     ss += swz_f<16>(ss); ss = sum_x32(ss);
;                     const float r = __builtin_amdgcn_rsqf(ss * (1.f / 64.f) + EPS) * gsc;
; #pragma unroll
;                     for (int bj = 0; bj < 2; ++bj)
; #pragma unroll
;                         for (int n = 0; n < 2; ++n) v[bj][n] = v[bj][n] * r * *(const f32x4*)(gp + 32 * bj + 4 * n);
;     ...
;                 bf16* rowp = U + (size_t)row * NIN + pn * BM + 64 * wc + 8 * fq;
; #pragma unroll
;                 for (int bj = 0; bj < 2; ++bj) *(u32x4*)(rowp + 32 * bj) = pack8(v[bj][0], v[bj][1]);
.LBB0_362:
	v_lshlrev_b32_e32 v112, 3, v179
	v_ashrrev_i32_e32 v113, 31, v112
	v_mov_b32_e32 v114, 0x3e38aa3b
	v_cndmask_b32_e64 v129, 1.0, v114, s[2:3]
	v_lshl_add_u64 v[114:115], v[112:113], 2, s[6:7]
	s_and_b64 vcc, exec, s[30:31]
	s_cbranch_vccz .LBB0_364
	v_pk_mul_f32 v[144:145], v[152:153], v[152:153]
	v_pk_mul_f32 v[146:147], v[154:155], v[154:155]
	s_nop 0
	v_pk_mov_b32 v[148:149], v[146:147], v[144:145] op_sel:[1,0]
	v_mov_b32_e32 v147, v145
	v_pk_add_f32 v[144:145], v[148:149], v[146:147]
	v_pk_mul_f32 v[146:147], v[122:123], v[122:123]
	v_pk_add_f32 v[144:145], v[144:145], v[144:145] op_sel_hi:[0,1]
	v_pk_mul_f32 v[148:149], v[124:125], v[124:125]
	v_mul_f32_e32 v144, v126, v126
	v_pk_mov_b32 v[150:151], v[148:149], v[146:147] op_sel:[1,0]
	v_mov_b32_e32 v149, v147
	v_pk_add_f32 v[146:147], v[150:151], v[148:149]
	v_pk_fma_f32 v[148:149], v[126:127], v[126:127], v[144:145] op_sel_hi:[1,1,0]
	v_mul_f32_e32 v144, v120, v120
	v_pk_add_f32 v[146:147], v[146:147], v[146:147] op_sel_hi:[0,1]
	v_pk_fma_f32 v[150:151], v[120:121], v[120:121], v[144:145] op_sel_hi:[1,1,0]
	v_mul_f32_e32 v148, v118, v118
	v_mul_f32_e32 v150, v119, v119
	v_mul_f32_e32 v144, v116, v116
	v_mul_f32_e32 v146, v117, v117
	v_pk_add_f32 v[148:149], v[148:149], v[150:151]
	v_pk_add_f32 v[144:145], v[144:145], v[146:147]
	s_nop 0
	v_pk_add_f32 v[144:145], v[148:149], v[144:145]
	s_nop 0
	v_add_f32_e32 v144, v144, v145
	ds_swizzle_b32 v145, v144 offset:swizzle(SWAP,16)
	s_waitcnt lgkmcnt(0)
	v_add_f32_e32 v144, v144, v145
	v_mov_b32_e32 v145, v144
	s_nop 1
	v_permlane32_swap_b32_e32 v144, v145
	v_add_f32_e32 v144, v144, v145
	v_fmamk_f32 v144, v144, 0x3c800000, v230
	v_rsq_f32_e32 v144, v144
	s_nop 0
	v_mul_f32_e32 v160, v129, v144
	v_pk_mul_f32 v[146:147], v[154:155], v[160:161] op_sel_hi:[1,0]
	v_pk_mul_f32 v[144:145], v[152:153], v[160:161] op_sel_hi:[1,0]
	global_load_dwordx4 v[180:183], v[114:115], off
	global_load_dwordx4 v[184:187], v[114:115], off offset:16
	global_load_dwordx4 v[188:191], v[114:115], off offset:128
	global_load_dwordx4 v[192:195], v[114:115], off offset:144
	global_load_dwordx4 v[148:151], v[114:115], off offset:16
	global_load_dwordx4 v[152:155], v[114:115], off
	v_pk_mul_f32 v[124:125], v[124:125], v[160:161] op_sel_hi:[1,0]
	v_pk_mul_f32 v[122:123], v[122:123], v[160:161] op_sel_hi:[1,0]
	v_pk_mul_f32 v[118:119], v[118:119], v[160:161] op_sel_hi:[1,0]
	v_pk_mul_f32 v[116:117], v[116:117], v[160:161] op_sel_hi:[1,0]
	s_waitcnt vmcnt(1)
	v_pk_mul_f32 v[150:151], v[150:151], v[122:123]
	s_waitcnt vmcnt(0)
	v_pk_mul_f32 v[144:145], v[154:155], v[144:145]
	v_pk_mul_f32 v[146:147], v[152:153], v[146:147]
	v_pk_mul_f32 v[148:149], v[148:149], v[124:125]
	v_pk_mul_f32 v[152:153], v[126:127], v[160:161] op_sel_hi:[1,0]
	v_pk_mul_f32 v[154:155], v[120:121], v[160:161] op_sel_hi:[1,0]
	global_load_dwordx4 v[120:123], v[114:115], off offset:144
	global_load_dwordx4 v[124:127], v[114:115], off offset:128
	s_waitcnt vmcnt(1)
	v_pk_mul_f32 v[160:161], v[122:123], v[116:117]
	s_waitcnt vmcnt(0)
	v_pk_mul_f32 v[156:157], v[126:127], v[154:155]
	v_pk_mul_f32 v[158:159], v[124:125], v[152:153]
	v_pk_mul_f32 v[162:163], v[120:121], v[118:119]

; template <int MASK> __device__ __forceinline__ float swz_f(float v) { return __builtin_bit_cast(float, __builtin_amdgcn_ds_swizzle(__builtin_bit_cast(int, v), (MASK << 10) | 0x1f)); }
; __device__ __forceinline__ float sum_x32(float v) { const unsigned u = __builtin_bit_cast(unsigned, v); auto rr = __builtin_amdgcn_permlane32_swap(u, u, false, false); return __builtin_bit_cast(float, (unsigned)rr[0]) + __builtin_bit_cast(float, (unsigned)rr[1]); }
;     __device__ __forceinline__ void operator()(const f32x4 (&acc)[2][2][4][2], const Unit& u, int wr, int wc, int fr, int fq) const {
;     ...
;                 if (!GATES && type <= 1) { float ss = 0.f;
; #pragma unroll
;                     for (int bj = 0; bj < 2; ++bj)
; #pragma unroll
;                         for (int n = 0; n < 2; ++n) ss += (v[bj][n][0] * v[bj][n][0] + v[bj][n][1] * v[bj][n][1]) + (v[bj][n][2] * v[bj][n][2] + v[bj][n][3] * v[bj][n][3]);
;                     ss += swz_f<16>(ss); ss = sum_x32(ss);
;                     const float r = __builtin_amdgcn_rsqf(ss * (1.f / 64.f) + EPS) * gsc;
; #pragma unroll
;                     for (int bj = 0; bj < 2; ++bj)
; #pragma unroll
;                         for (int n = 0; n < 2; ++n) v[bj][n] = v[bj][n] * r * *(const f32x4*)(gp + 32 * bj + 4 * n);
.LBB0_371:
	s_and_b64 vcc, exec, s[28:29]
	s_cbranch_vccz .LBB0_373
	v_pk_mul_f32 v[108:109], v[120:121], v[120:121]
	v_pk_mul_f32 v[110:111], v[122:123], v[122:123]
	s_nop 0
	v_pk_mov_b32 v[116:117], v[110:111], v[108:109] op_sel:[1,0]
	v_mov_b32_e32 v111, v109
	v_pk_add_f32 v[108:109], v[116:117], v[110:111]
	v_pk_mul_f32 v[110:111], v[106:107], v[106:107]
	v_pk_add_f32 v[108:109], v[108:109], v[108:109] op_sel_hi:[0,1]
	v_pk_mul_f32 v[116:117], v[104:105], v[104:105]
	v_mul_f32_e32 v108, v100, v100
	v_pk_mov_b32 v[118:119], v[116:117], v[110:111] op_sel:[1,0]
	v_mov_b32_e32 v117, v111
	v_pk_add_f32 v[110:111], v[118:119], v[116:117]
	v_pk_fma_f32 v[116:117], v[100:101], v[100:101], v[108:109] op_sel_hi:[1,1,0]
	v_mul_f32_e32 v108, v102, v102
	v_pk_add_f32 v[110:111], v[110:111], v[110:111] op_sel_hi:[0,1]
	v_pk_fma_f32 v[118:119], v[102:103], v[102:103], v[108:109] op_sel_hi:[1,1,0]
	v_mul_f32_e32 v116, v96, v96
	v_mul_f32_e32 v118, v97, v97
	v_mul_f32_e32 v108, v98, v98
	v_mul_f32_e32 v110, v99, v99
	v_pk_add_f32 v[116:117], v[116:117], v[118:119]
	v_pk_add_f32 v[108:109], v[108:109], v[110:111]
	s_nop 0
	v_pk_add_f32 v[108:109], v[116:117], v[108:109]
	s_nop 0
	v_add_f32_e32 v108, v108, v109
	ds_swizzle_b32 v109, v108 offset:swizzle(SWAP,16)
	s_waitcnt lgkmcnt(0)
	v_add_f32_e32 v108, v108, v109
	v_mov_b32_e32 v109, v108
	s_nop 1
	v_permlane32_swap_b32_e32 v108, v109
	v_add_f32_e32 v108, v108, v109
	v_fmamk_f32 v108, v108, 0x3c800000, v230
	v_rsq_f32_e32 v108, v108
	s_nop 0
	v_mul_f32_e32 v142, v129, v108
	v_pk_mul_f32 v[110:111], v[122:123], v[142:143] op_sel_hi:[1,0]
	v_pk_mul_f32 v[108:109], v[120:121], v[142:143] op_sel_hi:[1,0]
	v_mov_b32_e32 v116, v184
	v_mov_b32_e32 v117, v185
	v_mov_b32_e32 v118, v186
	v_mov_b32_e32 v119, v187
	v_mov_b32_e32 v120, v180
	v_mov_b32_e32 v121, v181
	v_mov_b32_e32 v122, v182
	v_mov_b32_e32 v123, v183
	v_pk_mul_f32 v[104:105], v[104:105], v[142:143] op_sel_hi:[1,0]
	v_pk_mul_f32 v[106:107], v[106:107], v[142:143] op_sel_hi:[1,0]
	v_pk_mul_f32 v[96:97], v[96:97], v[142:143] op_sel_hi:[1,0]
	v_pk_mul_f32 v[98:99], v[98:99], v[142:143] op_sel_hi:[1,0]
	s_nop 0
	v_pk_mul_f32 v[118:119], v[118:119], v[106:107]
	s_nop 0
	v_pk_mul_f32 v[108:109], v[122:123], v[108:109]
	v_pk_mul_f32 v[110:111], v[120:121], v[110:111]
	v_pk_mul_f32 v[116:117], v[116:117], v[104:105]
	v_pk_mul_f32 v[120:121], v[100:101], v[142:143] op_sel_hi:[1,0]
	v_pk_mul_f32 v[122:123], v[102:103], v[142:143] op_sel_hi:[1,0]
	v_mov_b32_e32 v100, v192
	v_mov_b32_e32 v101, v193
	v_mov_b32_e32 v102, v194
	v_mov_b32_e32 v103, v195
	v_mov_b32_e32 v104, v188
	v_mov_b32_e32 v105, v189
	v_mov_b32_e32 v106, v190
	v_mov_b32_e32 v107, v191
	s_nop 0
	v_pk_mul_f32 v[142:143], v[102:103], v[98:99]
	s_nop 0
	v_pk_mul_f32 v[124:125], v[106:107], v[122:123]
	v_pk_mul_f32 v[126:127], v[104:105], v[120:121]
	v_pk_mul_f32 v[144:145], v[100:101], v[96:97]

; template <int MASK> __device__ __forceinline__ float swz_f(float v) { return __builtin_bit_cast(float, __builtin_amdgcn_ds_swizzle(__builtin_bit_cast(int, v), (MASK << 10) | 0x1f)); }
; __device__ __forceinline__ float sum_x32(float v) { const unsigned u = __builtin_bit_cast(unsigned, v); auto rr = __builtin_amdgcn_permlane32_swap(u, u, false, false); return __builtin_bit_cast(float, (unsigned)rr[0]) + __builtin_bit_cast(float, (unsigned)rr[1]); }
;     __device__ __forceinline__ void operator()(const f32x4 (&acc)[2][2][4][2], const Unit& u, int wr, int wc, int fr, int fq) const {
;     ...
;                 if (!GATES && type <= 1) { float ss = 0.f;
; #pragma unroll
;                     for (int bj = 0; bj < 2; ++bj)
; #pragma unroll
;                         for (int n = 0; n < 2; ++n) ss += (v[bj][n][0] * v[bj][n][0] + v[bj][n][1] * v[bj][n][1]) + (v[bj][n][2] * v[bj][n][2] + v[bj][n][3] * v[bj][n][3]);
;                     ss += swz_f<16>(ss); ss = sum_x32(ss);
;                     const float r = __builtin_amdgcn_rsqf(ss * (1.f / 64.f) + EPS) * gsc;
; #pragma unroll
;                     for (int bj = 0; bj < 2; ++bj)
; #pragma unroll
;                         for (int n = 0; n < 2; ++n) v[bj][n] = v[bj][n] * r * *(const f32x4*)(gp + 32 * bj + 4 * n);
.LBB0_380:
	s_and_b64 vcc, exec, s[28:29]
	s_cbranch_vccz .LBB0_382
	v_pk_mul_f32 v[92:93], v[100:101], v[100:101]
	v_pk_mul_f32 v[94:95], v[102:103], v[102:103]
	s_nop 0
	v_pk_mov_b32 v[96:97], v[94:95], v[92:93] op_sel:[1,0]
	v_mov_b32_e32 v95, v93
	v_pk_add_f32 v[92:93], v[96:97], v[94:95]
	v_pk_mul_f32 v[94:95], v[90:91], v[90:91]
	v_pk_add_f32 v[92:93], v[92:93], v[92:93] op_sel_hi:[0,1]
	v_pk_mul_f32 v[96:97], v[88:89], v[88:89]
	v_mul_f32_e32 v92, v84, v84
	v_pk_mov_b32 v[98:99], v[96:97], v[94:95] op_sel:[1,0]
	v_mov_b32_e32 v97, v95
	v_pk_add_f32 v[94:95], v[98:99], v[96:97]
	v_pk_fma_f32 v[96:97], v[84:85], v[84:85], v[92:93] op_sel_hi:[1,1,0]
	v_mul_f32_e32 v92, v86, v86
	v_pk_add_f32 v[94:95], v[94:95], v[94:95] op_sel_hi:[0,1]
	v_pk_fma_f32 v[98:99], v[86:87], v[86:87], v[92:93] op_sel_hi:[1,1,0]
	v_mul_f32_e32 v96, v80, v80
	v_mul_f32_e32 v98, v81, v81
	v_mul_f32_e32 v92, v82, v82
	v_mul_f32_e32 v94, v83, v83
	v_pk_add_f32 v[96:97], v[96:97], v[98:99]
	v_pk_add_f32 v[92:93], v[92:93], v[94:95]
	s_nop 0
	v_pk_add_f32 v[92:93], v[96:97], v[92:93]
	s_nop 0
	v_add_f32_e32 v92, v92, v93
	ds_swizzle_b32 v93, v92 offset:swizzle(SWAP,16)
	s_waitcnt lgkmcnt(0)
	v_add_f32_e32 v92, v92, v93
	v_mov_b32_e32 v93, v92
	s_nop 1
	v_permlane32_swap_b32_e32 v92, v93
	v_add_f32_e32 v92, v92, v93
	v_fmamk_f32 v92, v92, 0x3c800000, v230
	v_rsq_f32_e32 v92, v92
	s_nop 0
	v_mul_f32_e32 v108, v129, v92
	v_pk_mul_f32 v[94:95], v[102:103], v[108:109] op_sel_hi:[1,0]
	v_pk_mul_f32 v[92:93], v[100:101], v[108:109] op_sel_hi:[1,0]
	v_mov_b32_e32 v96, v184
	v_mov_b32_e32 v97, v185
	v_mov_b32_e32 v98, v186
	v_mov_b32_e32 v99, v187
	v_mov_b32_e32 v100, v180
	v_mov_b32_e32 v101, v181
	v_mov_b32_e32 v102, v182
	v_mov_b32_e32 v103, v183
	v_pk_mul_f32 v[88:89], v[88:89], v[108:109] op_sel_hi:[1,0]
	v_pk_mul_f32 v[90:91], v[90:91], v[108:109] op_sel_hi:[1,0]
	v_pk_mul_f32 v[80:81], v[80:81], v[108:109] op_sel_hi:[1,0]
	v_pk_mul_f32 v[82:83], v[82:83], v[108:109] op_sel_hi:[1,0]
	s_nop 0
	v_pk_mul_f32 v[98:99], v[98:99], v[90:91]
	s_nop 0
	v_pk_mul_f32 v[92:93], v[102:103], v[92:93]
	v_pk_mul_f32 v[94:95], v[100:101], v[94:95]
	v_pk_mul_f32 v[96:97], v[96:97], v[88:89]
	v_pk_mul_f32 v[100:101], v[84:85], v[108:109] op_sel_hi:[1,0]
	v_pk_mul_f32 v[102:103], v[86:87], v[108:109] op_sel_hi:[1,0]
	v_mov_b32_e32 v84, v192
	v_mov_b32_e32 v85, v193
	v_mov_b32_e32 v86, v194
	v_mov_b32_e32 v87, v195
	v_mov_b32_e32 v88, v188
	v_mov_b32_e32 v89, v189
	v_mov_b32_e32 v90, v190
	v_mov_b32_e32 v91, v191
	s_nop 0
	v_pk_mul_f32 v[108:109], v[86:87], v[82:83]
	s_nop 0
	v_pk_mul_f32 v[104:105], v[90:91], v[102:103]
	v_pk_mul_f32 v[106:107], v[88:89], v[100:101]
	v_pk_mul_f32 v[110:111], v[84:85], v[80:81]

; template <int MASK> __device__ __forceinline__ float swz_f(float v) { return __builtin_bit_cast(float, __builtin_amdgcn_ds_swizzle(__builtin_bit_cast(int, v), (MASK << 10) | 0x1f)); }
; __device__ __forceinline__ float sum_x32(float v) { const unsigned u = __builtin_bit_cast(unsigned, v); auto rr = __builtin_amdgcn_permlane32_swap(u, u, false, false); return __builtin_bit_cast(float, (unsigned)rr[0]) + __builtin_bit_cast(float, (unsigned)rr[1]); }
;     __device__ __forceinline__ void operator()(const f32x4 (&acc)[2][2][4][2], const Unit& u, int wr, int wc, int fr, int fq) const {
;     ...
;                 if (!GATES && type <= 1) { float ss = 0.f;
; #pragma unroll
;                     for (int bj = 0; bj < 2; ++bj)
; #pragma unroll
;                         for (int n = 0; n < 2; ++n) ss += (v[bj][n][0] * v[bj][n][0] + v[bj][n][1] * v[bj][n][1]) + (v[bj][n][2] * v[bj][n][2] + v[bj][n][3] * v[bj][n][3]);
;                     ss += swz_f<16>(ss); ss = sum_x32(ss);
;                     const float r = __builtin_amdgcn_rsqf(ss * (1.f / 64.f) + EPS) * gsc;
; #pragma unroll
;                     for (int bj = 0; bj < 2; ++bj)
; #pragma unroll
;                         for (int n = 0; n < 2; ++n) v[bj][n] = v[bj][n] * r * *(const f32x4*)(gp + 32 * bj + 4 * n);
.LBB0_389:
	s_and_b64 vcc, exec, s[28:29]
	s_cbranch_vccz .LBB0_391
	v_pk_mul_f32 v[76:77], v[84:85], v[84:85]
	v_pk_mul_f32 v[78:79], v[86:87], v[86:87]
	s_nop 0
	v_pk_mov_b32 v[80:81], v[78:79], v[76:77] op_sel:[1,0]
	v_mov_b32_e32 v79, v77
	v_pk_add_f32 v[76:77], v[80:81], v[78:79]
	v_pk_mul_f32 v[78:79], v[74:75], v[74:75]
	v_pk_add_f32 v[76:77], v[76:77], v[76:77] op_sel_hi:[0,1]
	v_pk_mul_f32 v[80:81], v[72:73], v[72:73]
	v_mul_f32_e32 v76, v68, v68
	v_pk_mov_b32 v[82:83], v[80:81], v[78:79] op_sel:[1,0]
	v_mov_b32_e32 v81, v79
	v_pk_add_f32 v[78:79], v[82:83], v[80:81]
	v_pk_fma_f32 v[80:81], v[68:69], v[68:69], v[76:77] op_sel_hi:[1,1,0]
	v_mul_f32_e32 v76, v70, v70
	v_pk_add_f32 v[78:79], v[78:79], v[78:79] op_sel_hi:[0,1]
	v_pk_fma_f32 v[82:83], v[70:71], v[70:71], v[76:77] op_sel_hi:[1,1,0]
	v_mul_f32_e32 v80, v64, v64
	v_mul_f32_e32 v82, v65, v65
	v_mul_f32_e32 v76, v66, v66
	v_mul_f32_e32 v78, v67, v67
	v_pk_add_f32 v[80:81], v[80:81], v[82:83]
	v_pk_add_f32 v[76:77], v[76:77], v[78:79]
	s_nop 0
	v_pk_add_f32 v[76:77], v[80:81], v[76:77]
	s_nop 0
	v_add_f32_e32 v76, v76, v77
	ds_swizzle_b32 v77, v76 offset:swizzle(SWAP,16)
	s_waitcnt lgkmcnt(0)
	v_add_f32_e32 v76, v76, v77
	v_mov_b32_e32 v77, v76
	s_nop 1
	v_permlane32_swap_b32_e32 v76, v77
	v_add_f32_e32 v76, v76, v77
	v_fmamk_f32 v76, v76, 0x3c800000, v230
	v_rsq_f32_e32 v76, v76
	s_nop 0
	v_mul_f32_e32 v92, v129, v76
	v_pk_mul_f32 v[78:79], v[86:87], v[92:93] op_sel_hi:[1,0]
	v_pk_mul_f32 v[76:77], v[84:85], v[92:93] op_sel_hi:[1,0]
	v_mov_b32_e32 v80, v184
	v_mov_b32_e32 v81, v185
	v_mov_b32_e32 v82, v186
	v_mov_b32_e32 v83, v187
	v_mov_b32_e32 v84, v180
	v_mov_b32_e32 v85, v181
	v_mov_b32_e32 v86, v182
	v_mov_b32_e32 v87, v183
	v_pk_mul_f32 v[72:73], v[72:73], v[92:93] op_sel_hi:[1,0]
	v_pk_mul_f32 v[74:75], v[74:75], v[92:93] op_sel_hi:[1,0]
	v_pk_mul_f32 v[64:65], v[64:65], v[92:93] op_sel_hi:[1,0]
	v_pk_mul_f32 v[66:67], v[66:67], v[92:93] op_sel_hi:[1,0]
	s_nop 0
	v_pk_mul_f32 v[82:83], v[82:83], v[74:75]
	s_nop 0
	v_pk_mul_f32 v[76:77], v[86:87], v[76:77]
	v_pk_mul_f32 v[78:79], v[84:85], v[78:79]
	v_pk_mul_f32 v[80:81], v[80:81], v[72:73]
	v_pk_mul_f32 v[84:85], v[68:69], v[92:93] op_sel_hi:[1,0]
	v_pk_mul_f32 v[86:87], v[70:71], v[92:93] op_sel_hi:[1,0]
	v_mov_b32_e32 v68, v192
	v_mov_b32_e32 v69, v193
	v_mov_b32_e32 v70, v194
	v_mov_b32_e32 v71, v195
	v_mov_b32_e32 v72, v188
	v_mov_b32_e32 v73, v189
	v_mov_b32_e32 v74, v190
	v_mov_b32_e32 v75, v191
	s_nop 0
	v_pk_mul_f32 v[92:93], v[70:71], v[66:67]
	s_nop 0
	v_pk_mul_f32 v[88:89], v[74:75], v[86:87]
	v_pk_mul_f32 v[90:91], v[72:73], v[84:85]
	v_pk_mul_f32 v[94:95], v[68:69], v[64:65]

; template <int MASK> __device__ __forceinline__ float swz_f(float v) { return __builtin_bit_cast(float, __builtin_amdgcn_ds_swizzle(__builtin_bit_cast(int, v), (MASK << 10) | 0x1f)); }
; __device__ __forceinline__ float sum_x32(float v) { const unsigned u = __builtin_bit_cast(unsigned, v); auto rr = __builtin_amdgcn_permlane32_swap(u, u, false, false); return __builtin_bit_cast(float, (unsigned)rr[0]) + __builtin_bit_cast(float, (unsigned)rr[1]); }
;     __device__ __forceinline__ void operator()(const f32x4 (&acc)[2][2][4][2], const Unit& u, int wr, int wc, int fr, int fq) const {
;     ...
;                 if (!GATES && type <= 1) { float ss = 0.f;
; #pragma unroll
;                     for (int bj = 0; bj < 2; ++bj)
; #pragma unroll
;                         for (int n = 0; n < 2; ++n) ss += (v[bj][n][0] * v[bj][n][0] + v[bj][n][1] * v[bj][n][1]) + (v[bj][n][2] * v[bj][n][2] + v[bj][n][3] * v[bj][n][3]);
;                     ss += swz_f<16>(ss); ss = sum_x32(ss);
;                     const float r = __builtin_amdgcn_rsqf(ss * (1.f / 64.f) + EPS) * gsc;
; #pragma unroll
;                     for (int bj = 0; bj < 2; ++bj)
; #pragma unroll
;                         for (int n = 0; n < 2; ++n) v[bj][n] = v[bj][n] * r * *(const f32x4*)(gp + 32 * bj + 4 * n);
.LBB0_398:
	s_and_b64 vcc, exec, s[28:29]
	s_cbranch_vccz .LBB0_400
	v_pk_mul_f32 v[60:61], v[68:69], v[68:69]
	v_pk_mul_f32 v[62:63], v[70:71], v[70:71]
	s_nop 0
	v_pk_mov_b32 v[64:65], v[62:63], v[60:61] op_sel:[1,0]
	v_mov_b32_e32 v63, v61
	v_pk_add_f32 v[60:61], v[64:65], v[62:63]
	v_pk_mul_f32 v[62:63], v[58:59], v[58:59]
	v_pk_add_f32 v[60:61], v[60:61], v[60:61] op_sel_hi:[0,1]
	v_pk_mul_f32 v[64:65], v[56:57], v[56:57]
	v_mul_f32_e32 v60, v52, v52
	v_pk_mov_b32 v[66:67], v[64:65], v[62:63] op_sel:[1,0]
	v_mov_b32_e32 v65, v63
	v_pk_add_f32 v[62:63], v[66:67], v[64:65]
	v_pk_fma_f32 v[64:65], v[52:53], v[52:53], v[60:61] op_sel_hi:[1,1,0]
	v_mul_f32_e32 v60, v54, v54
	v_pk_add_f32 v[62:63], v[62:63], v[62:63] op_sel_hi:[0,1]
	v_pk_fma_f32 v[66:67], v[54:55], v[54:55], v[60:61] op_sel_hi:[1,1,0]
	v_mul_f32_e32 v64, v48, v48
	v_mul_f32_e32 v66, v49, v49
	v_mul_f32_e32 v60, v50, v50
	v_mul_f32_e32 v62, v51, v51
	v_pk_add_f32 v[64:65], v[64:65], v[66:67]
	v_pk_add_f32 v[60:61], v[60:61], v[62:63]
	s_nop 0
	v_pk_add_f32 v[60:61], v[64:65], v[60:61]
	s_nop 0
	v_add_f32_e32 v60, v60, v61
	ds_swizzle_b32 v61, v60 offset:swizzle(SWAP,16)
	s_waitcnt lgkmcnt(0)
	v_add_f32_e32 v60, v60, v61
	v_mov_b32_e32 v61, v60
	s_nop 1
	v_permlane32_swap_b32_e32 v60, v61
	v_add_f32_e32 v60, v60, v61
	v_fmamk_f32 v60, v60, 0x3c800000, v230
	v_rsq_f32_e32 v60, v60
	s_nop 0
	v_mul_f32_e32 v76, v129, v60
	v_pk_mul_f32 v[62:63], v[70:71], v[76:77] op_sel_hi:[1,0]
	v_pk_mul_f32 v[60:61], v[68:69], v[76:77] op_sel_hi:[1,0]
	v_mov_b32_e32 v64, v184
	v_mov_b32_e32 v65, v185
	v_mov_b32_e32 v66, v186
	v_mov_b32_e32 v67, v187
	v_mov_b32_e32 v68, v180
	v_mov_b32_e32 v69, v181
	v_mov_b32_e32 v70, v182
	v_mov_b32_e32 v71, v183
	v_pk_mul_f32 v[56:57], v[56:57], v[76:77] op_sel_hi:[1,0]
	v_pk_mul_f32 v[58:59], v[58:59], v[76:77] op_sel_hi:[1,0]
	v_pk_mul_f32 v[48:49], v[48:49], v[76:77] op_sel_hi:[1,0]
	v_pk_mul_f32 v[50:51], v[50:51], v[76:77] op_sel_hi:[1,0]
	s_nop 0
	v_pk_mul_f32 v[66:67], v[66:67], v[58:59]
	s_nop 0
	v_pk_mul_f32 v[60:61], v[70:71], v[60:61]
	v_pk_mul_f32 v[62:63], v[68:69], v[62:63]
	v_pk_mul_f32 v[64:65], v[64:65], v[56:57]
	v_pk_mul_f32 v[68:69], v[52:53], v[76:77] op_sel_hi:[1,0]
	v_pk_mul_f32 v[70:71], v[54:55], v[76:77] op_sel_hi:[1,0]
	v_mov_b32_e32 v52, v192
	v_mov_b32_e32 v53, v193
	v_mov_b32_e32 v54, v194
	v_mov_b32_e32 v55, v195
	v_mov_b32_e32 v56, v188
	v_mov_b32_e32 v57, v189
	v_mov_b32_e32 v58, v190
	v_mov_b32_e32 v59, v191
	s_nop 0
	v_pk_mul_f32 v[76:77], v[54:55], v[50:51]
	s_nop 0
	v_pk_mul_f32 v[72:73], v[58:59], v[70:71]
	v_pk_mul_f32 v[74:75], v[56:57], v[68:69]
	v_pk_mul_f32 v[78:79], v[52:53], v[48:49]

; template <int MASK> __device__ __forceinline__ float swz_f(float v) { return __builtin_bit_cast(float, __builtin_amdgcn_ds_swizzle(__builtin_bit_cast(int, v), (MASK << 10) | 0x1f)); }
; __device__ __forceinline__ float sum_x32(float v) { const unsigned u = __builtin_bit_cast(unsigned, v); auto rr = __builtin_amdgcn_permlane32_swap(u, u, false, false); return __builtin_bit_cast(float, (unsigned)rr[0]) + __builtin_bit_cast(float, (unsigned)rr[1]); }
;     __device__ __forceinline__ void operator()(const f32x4 (&acc)[2][2][4][2], const Unit& u, int wr, int wc, int fr, int fq) const {
;     ...
;                 if (!GATES && type <= 1) { float ss = 0.f;
; #pragma unroll
;                     for (int bj = 0; bj < 2; ++bj)
; #pragma unroll
;                         for (int n = 0; n < 2; ++n) ss += (v[bj][n][0] * v[bj][n][0] + v[bj][n][1] * v[bj][n][1]) + (v[bj][n][2] * v[bj][n][2] + v[bj][n][3] * v[bj][n][3]);
;                     ss += swz_f<16>(ss); ss = sum_x32(ss);
;                     const float r = __builtin_amdgcn_rsqf(ss * (1.f / 64.f) + EPS) * gsc;
; #pragma unroll
;                     for (int bj = 0; bj < 2; ++bj)
; #pragma unroll
;                         for (int n = 0; n < 2; ++n) v[bj][n] = v[bj][n] * r * *(const f32x4*)(gp + 32 * bj + 4 * n);
.LBB0_407:
	s_and_b64 vcc, exec, s[28:29]
	s_cbranch_vccz .LBB0_409
	v_pk_mul_f32 v[44:45], v[52:53], v[52:53]
	v_pk_mul_f32 v[46:47], v[54:55], v[54:55]
	s_nop 0
	v_pk_mov_b32 v[48:49], v[46:47], v[44:45] op_sel:[1,0]
	v_mov_b32_e32 v47, v45
	v_pk_add_f32 v[44:45], v[48:49], v[46:47]
	v_pk_mul_f32 v[46:47], v[42:43], v[42:43]
	v_pk_add_f32 v[44:45], v[44:45], v[44:45] op_sel_hi:[0,1]
	v_pk_mul_f32 v[48:49], v[40:41], v[40:41]
	v_mul_f32_e32 v44, v36, v36
	v_pk_mov_b32 v[50:51], v[48:49], v[46:47] op_sel:[1,0]
	v_mov_b32_e32 v49, v47
	v_pk_add_f32 v[46:47], v[50:51], v[48:49]
	v_pk_fma_f32 v[48:49], v[36:37], v[36:37], v[44:45] op_sel_hi:[1,1,0]
	v_mul_f32_e32 v44, v38, v38
	v_pk_add_f32 v[46:47], v[46:47], v[46:47] op_sel_hi:[0,1]
	v_pk_fma_f32 v[50:51], v[38:39], v[38:39], v[44:45] op_sel_hi:[1,1,0]
	v_mul_f32_e32 v48, v32, v32
	v_mul_f32_e32 v50, v33, v33
	v_mul_f32_e32 v44, v34, v34
	v_mul_f32_e32 v46, v35, v35
	v_pk_add_f32 v[48:49], v[48:49], v[50:51]
	v_pk_add_f32 v[44:45], v[44:45], v[46:47]
	s_nop 0
	v_pk_add_f32 v[44:45], v[48:49], v[44:45]
	s_nop 0
	v_add_f32_e32 v44, v44, v45
	ds_swizzle_b32 v45, v44 offset:swizzle(SWAP,16)
	s_waitcnt lgkmcnt(0)
	v_add_f32_e32 v44, v44, v45
	v_mov_b32_e32 v45, v44
	s_nop 1
	v_permlane32_swap_b32_e32 v44, v45
	v_add_f32_e32 v44, v44, v45
	v_fmamk_f32 v44, v44, 0x3c800000, v230
	v_rsq_f32_e32 v44, v44
	s_nop 0
	v_mul_f32_e32 v60, v129, v44
	v_pk_mul_f32 v[46:47], v[54:55], v[60:61] op_sel_hi:[1,0]
	v_pk_mul_f32 v[44:45], v[52:53], v[60:61] op_sel_hi:[1,0]
	v_mov_b32_e32 v48, v184
	v_mov_b32_e32 v49, v185
	v_mov_b32_e32 v50, v186
	v_mov_b32_e32 v51, v187
	v_mov_b32_e32 v52, v180
	v_mov_b32_e32 v53, v181
	v_mov_b32_e32 v54, v182
	v_mov_b32_e32 v55, v183
	v_pk_mul_f32 v[40:41], v[40:41], v[60:61] op_sel_hi:[1,0]
	v_pk_mul_f32 v[42:43], v[42:43], v[60:61] op_sel_hi:[1,0]
	v_pk_mul_f32 v[32:33], v[32:33], v[60:61] op_sel_hi:[1,0]
	v_pk_mul_f32 v[34:35], v[34:35], v[60:61] op_sel_hi:[1,0]
	s_nop 0
	v_pk_mul_f32 v[50:51], v[50:51], v[42:43]
	s_nop 0
	v_pk_mul_f32 v[44:45], v[54:55], v[44:45]
	v_pk_mul_f32 v[46:47], v[52:53], v[46:47]
	v_pk_mul_f32 v[48:49], v[48:49], v[40:41]
	v_pk_mul_f32 v[52:53], v[36:37], v[60:61] op_sel_hi:[1,0]
	v_pk_mul_f32 v[54:55], v[38:39], v[60:61] op_sel_hi:[1,0]
	v_mov_b32_e32 v36, v192
	v_mov_b32_e32 v37, v193
	v_mov_b32_e32 v38, v194
	v_mov_b32_e32 v39, v195
	v_mov_b32_e32 v40, v188
	v_mov_b32_e32 v41, v189
	v_mov_b32_e32 v42, v190
	v_mov_b32_e32 v43, v191
	s_nop 0
	v_pk_mul_f32 v[60:61], v[38:39], v[34:35]
	s_nop 0
	v_pk_mul_f32 v[56:57], v[42:43], v[54:55]
	v_pk_mul_f32 v[58:59], v[40:41], v[52:53]
	v_pk_mul_f32 v[62:63], v[36:37], v[32:33]

; template <int MASK> __device__ __forceinline__ float swz_f(float v) { return __builtin_bit_cast(float, __builtin_amdgcn_ds_swizzle(__builtin_bit_cast(int, v), (MASK << 10) | 0x1f)); }
; __device__ __forceinline__ float sum_x32(float v) { const unsigned u = __builtin_bit_cast(unsigned, v); auto rr = __builtin_amdgcn_permlane32_swap(u, u, false, false); return __builtin_bit_cast(float, (unsigned)rr[0]) + __builtin_bit_cast(float, (unsigned)rr[1]); }
;     __device__ __forceinline__ void operator()(const f32x4 (&acc)[2][2][4][2], const Unit& u, int wr, int wc, int fr, int fq) const {
;     ...
;                 if (!GATES && type <= 1) { float ss = 0.f;
; #pragma unroll
;                     for (int bj = 0; bj < 2; ++bj)
; #pragma unroll
;                         for (int n = 0; n < 2; ++n) ss += (v[bj][n][0] * v[bj][n][0] + v[bj][n][1] * v[bj][n][1]) + (v[bj][n][2] * v[bj][n][2] + v[bj][n][3] * v[bj][n][3]);
;                     ss += swz_f<16>(ss); ss = sum_x32(ss);
;                     const float r = __builtin_amdgcn_rsqf(ss * (1.f / 64.f) + EPS) * gsc;
; #pragma unroll
;                     for (int bj = 0; bj < 2; ++bj)
; #pragma unroll
;                         for (int n = 0; n < 2; ++n) v[bj][n] = v[bj][n] * r * *(const f32x4*)(gp + 32 * bj + 4 * n);
.LBB0_416:
	s_and_b64 vcc, exec, s[28:29]
	s_cbranch_vccz .LBB0_418
	v_pk_mul_f32 v[28:29], v[36:37], v[36:37]
	v_pk_mul_f32 v[30:31], v[38:39], v[38:39]
	s_nop 0
	v_pk_mov_b32 v[32:33], v[30:31], v[28:29] op_sel:[1,0]
	v_mov_b32_e32 v31, v29
	v_pk_add_f32 v[28:29], v[32:33], v[30:31]
	v_pk_mul_f32 v[30:31], v[26:27], v[26:27]
	v_pk_add_f32 v[28:29], v[28:29], v[28:29] op_sel_hi:[0,1]
	v_pk_mul_f32 v[32:33], v[24:25], v[24:25]
	v_mul_f32_e32 v28, v20, v20
	v_pk_mov_b32 v[34:35], v[32:33], v[30:31] op_sel:[1,0]
	v_mov_b32_e32 v33, v31
	v_pk_add_f32 v[30:31], v[34:35], v[32:33]
	v_pk_fma_f32 v[32:33], v[20:21], v[20:21], v[28:29] op_sel_hi:[1,1,0]
	v_mul_f32_e32 v28, v22, v22
	v_pk_add_f32 v[30:31], v[30:31], v[30:31] op_sel_hi:[0,1]
	v_pk_fma_f32 v[34:35], v[22:23], v[22:23], v[28:29] op_sel_hi:[1,1,0]
	v_mul_f32_e32 v32, v16, v16
	v_mul_f32_e32 v34, v17, v17
	v_mul_f32_e32 v28, v18, v18
	v_mul_f32_e32 v30, v19, v19
	v_pk_add_f32 v[32:33], v[32:33], v[34:35]
	v_pk_add_f32 v[28:29], v[28:29], v[30:31]
	s_nop 0
	v_pk_add_f32 v[28:29], v[32:33], v[28:29]
	s_nop 0
	v_add_f32_e32 v28, v28, v29
	ds_swizzle_b32 v29, v28 offset:swizzle(SWAP,16)
	s_waitcnt lgkmcnt(0)
	v_add_f32_e32 v28, v28, v29
	v_mov_b32_e32 v29, v28
	s_nop 1
	v_permlane32_swap_b32_e32 v28, v29
	v_add_f32_e32 v28, v28, v29
	v_fmamk_f32 v28, v28, 0x3c800000, v230
	v_rsq_f32_e32 v28, v28
	s_nop 0
	v_mul_f32_e32 v44, v129, v28
	v_pk_mul_f32 v[30:31], v[38:39], v[44:45] op_sel_hi:[1,0]
	v_pk_mul_f32 v[28:29], v[36:37], v[44:45] op_sel_hi:[1,0]
	v_mov_b32_e32 v32, v184
	v_mov_b32_e32 v33, v185
	v_mov_b32_e32 v34, v186
	v_mov_b32_e32 v35, v187
	v_mov_b32_e32 v36, v180
	v_mov_b32_e32 v37, v181
	v_mov_b32_e32 v38, v182
	v_mov_b32_e32 v39, v183
	v_pk_mul_f32 v[24:25], v[24:25], v[44:45] op_sel_hi:[1,0]
	v_pk_mul_f32 v[26:27], v[26:27], v[44:45] op_sel_hi:[1,0]
	v_pk_mul_f32 v[16:17], v[16:17], v[44:45] op_sel_hi:[1,0]
	v_pk_mul_f32 v[18:19], v[18:19], v[44:45] op_sel_hi:[1,0]
	s_nop 0
	v_pk_mul_f32 v[34:35], v[34:35], v[26:27]
	s_nop 0
	v_pk_mul_f32 v[28:29], v[38:39], v[28:29]
	v_pk_mul_f32 v[30:31], v[36:37], v[30:31]
	v_pk_mul_f32 v[32:33], v[32:33], v[24:25]
	v_pk_mul_f32 v[36:37], v[20:21], v[44:45] op_sel_hi:[1,0]
	v_pk_mul_f32 v[38:39], v[22:23], v[44:45] op_sel_hi:[1,0]
	v_mov_b32_e32 v20, v192
	v_mov_b32_e32 v21, v193
	v_mov_b32_e32 v22, v194
	v_mov_b32_e32 v23, v195
	v_mov_b32_e32 v24, v188
	v_mov_b32_e32 v25, v189
	v_mov_b32_e32 v26, v190
	v_mov_b32_e32 v27, v191
	s_nop 0
	v_pk_mul_f32 v[44:45], v[22:23], v[18:19]
	s_nop 0
	v_pk_mul_f32 v[40:41], v[26:27], v[38:39]
	v_pk_mul_f32 v[42:43], v[24:25], v[36:37]
	v_pk_mul_f32 v[46:47], v[20:21], v[16:17]

; template <int MASK> __device__ __forceinline__ float swz_f(float v) { return __builtin_bit_cast(float, __builtin_amdgcn_ds_swizzle(__builtin_bit_cast(int, v), (MASK << 10) | 0x1f)); }
; __device__ __forceinline__ float sum_x32(float v) { const unsigned u = __builtin_bit_cast(unsigned, v); auto rr = __builtin_amdgcn_permlane32_swap(u, u, false, false); return __builtin_bit_cast(float, (unsigned)rr[0]) + __builtin_bit_cast(float, (unsigned)rr[1]); }
;     __device__ __forceinline__ void operator()(const f32x4 (&acc)[2][2][4][2], const Unit& u, int wr, int wc, int fr, int fq) const {
;     ...
;                 if (!GATES && type <= 1) { float ss = 0.f;
; #pragma unroll
;                     for (int bj = 0; bj < 2; ++bj)
; #pragma unroll
;                         for (int n = 0; n < 2; ++n) ss += (v[bj][n][0] * v[bj][n][0] + v[bj][n][1] * v[bj][n][1]) + (v[bj][n][2] * v[bj][n][2] + v[bj][n][3] * v[bj][n][3]);
;                     ss += swz_f<16>(ss); ss = sum_x32(ss);
;                     const float r = __builtin_amdgcn_rsqf(ss * (1.f / 64.f) + EPS) * gsc;
; #pragma unroll
;                     for (int bj = 0; bj < 2; ++bj)
; #pragma unroll
;                         for (int n = 0; n < 2; ++n) v[bj][n] = v[bj][n] * r * *(const f32x4*)(gp + 32 * bj + 4 * n);
.LBB0_425:
	s_and_b64 vcc, exec, s[2:3]
	s_cbranch_vccz .LBB0_427
	v_pk_mul_f32 v[12:13], v[20:21], v[20:21]
	v_pk_mul_f32 v[14:15], v[22:23], v[22:23]
	s_nop 0
	v_pk_mov_b32 v[16:17], v[14:15], v[12:13] op_sel:[1,0]
	v_mov_b32_e32 v15, v13
	v_pk_add_f32 v[12:13], v[16:17], v[14:15]
	v_pk_mul_f32 v[14:15], v[10:11], v[10:11]
	v_pk_add_f32 v[12:13], v[12:13], v[12:13] op_sel_hi:[0,1]
	v_pk_mul_f32 v[16:17], v[8:9], v[8:9]
	v_mul_f32_e32 v12, v4, v4
	v_pk_mov_b32 v[18:19], v[16:17], v[14:15] op_sel:[1,0]
	v_mov_b32_e32 v17, v15
	v_pk_add_f32 v[14:15], v[18:19], v[16:17]
	v_pk_fma_f32 v[16:17], v[4:5], v[4:5], v[12:13] op_sel_hi:[1,1,0]
	v_mul_f32_e32 v12, v6, v6
	v_pk_add_f32 v[14:15], v[14:15], v[14:15] op_sel_hi:[0,1]
	v_pk_fma_f32 v[18:19], v[6:7], v[6:7], v[12:13] op_sel_hi:[1,1,0]
	v_mul_f32_e32 v16, v0, v0
	v_mul_f32_e32 v18, v1, v1
	v_mul_f32_e32 v12, v2, v2
	v_mul_f32_e32 v14, v3, v3
	v_pk_add_f32 v[16:17], v[16:17], v[18:19]
	v_pk_add_f32 v[12:13], v[12:13], v[14:15]
	s_nop 0
	v_pk_add_f32 v[12:13], v[16:17], v[12:13]
	s_nop 0
	v_add_f32_e32 v12, v12, v13
	ds_swizzle_b32 v13, v12 offset:swizzle(SWAP,16)
	s_waitcnt lgkmcnt(0)
	v_add_f32_e32 v12, v12, v13
	v_mov_b32_e32 v13, v12
	s_nop 1
	v_permlane32_swap_b32_e32 v12, v13
	v_add_f32_e32 v12, v12, v13
	v_fmamk_f32 v12, v12, 0x3c800000, v230
	v_rsq_f32_e32 v12, v12
	s_nop 0
	v_mul_f32_e32 v28, v129, v12
	v_pk_mul_f32 v[14:15], v[22:23], v[28:29] op_sel_hi:[1,0]
	v_pk_mul_f32 v[12:13], v[20:21], v[28:29] op_sel_hi:[1,0]
	v_mov_b32_e32 v16, v184
	v_mov_b32_e32 v17, v185
	v_mov_b32_e32 v18, v186
	v_mov_b32_e32 v19, v187
	v_mov_b32_e32 v20, v180
	v_mov_b32_e32 v21, v181
	v_mov_b32_e32 v22, v182
	v_mov_b32_e32 v23, v183
	v_pk_mul_f32 v[8:9], v[8:9], v[28:29] op_sel_hi:[1,0]
	v_pk_mul_f32 v[10:11], v[10:11], v[28:29] op_sel_hi:[1,0]
	v_pk_mul_f32 v[0:1], v[0:1], v[28:29] op_sel_hi:[1,0]
	v_pk_mul_f32 v[2:3], v[2:3], v[28:29] op_sel_hi:[1,0]
	s_nop 0
	v_pk_mul_f32 v[18:19], v[18:19], v[10:11]
	s_nop 0
	v_pk_mul_f32 v[12:13], v[22:23], v[12:13]
	v_pk_mul_f32 v[14:15], v[20:21], v[14:15]
	v_pk_mul_f32 v[16:17], v[16:17], v[8:9]
	v_pk_mul_f32 v[20:21], v[4:5], v[28:29] op_sel_hi:[1,0]
	v_pk_mul_f32 v[22:23], v[6:7], v[28:29] op_sel_hi:[1,0]
	v_mov_b32_e32 v4, v192
	v_mov_b32_e32 v5, v193
	v_mov_b32_e32 v6, v194
	v_mov_b32_e32 v7, v195
	v_mov_b32_e32 v8, v188
	v_mov_b32_e32 v9, v189
	v_mov_b32_e32 v10, v190
	v_mov_b32_e32 v11, v191
	s_nop 0
	v_pk_mul_f32 v[28:29], v[6:7], v[2:3]
	s_nop 0
	v_pk_mul_f32 v[24:25], v[10:11], v[22:23]
	v_pk_mul_f32 v[26:27], v[8:9], v[20:21]
	v_pk_mul_f32 v[30:31], v[4:5], v[0:1]

;     __device__ __forceinline__ bool next(int i, Unit& u) const { return so.next(i, u); }
;     __device__ __forceinline__ void setup(int G_, int c_) { so.setup(G_, c_); }
;     __device__ __forceinline__ bool next(int i, Unit& u) const { const bool ok = so.next(i >> 1, u); u.part = i & 1; return ok; }
;     __host__ __device__ bool next(int i, Unit& u) const {
;         const int L = i * G + c; if (L >= nwg) return false;
;         int wgid = L; { const int q = nwg / NXCD, r = nwg % NXCD, xcd = wgid % NXCD, off = wgid / NXCD; wgid = (xcd < r ? xcd * (q + 1) : r * (q + 1) + (xcd - r) * q) + off; }
;         const int nig = WGM * nN, gid = wgid / nig, fm = gid * WGM, gsz = (nM - fm) < WGM ? (nM - fm) : WGM;
;         u.pm = fm + ((wgid % nig) % gsz); u.pn = (wgid % nig) / gsz; u.part = 0; return true;
;     __device__ __forceinline__ void setup(int G_, int c_) {
; #pragma unroll
;         for (int e = 0; e < 9; ++e) ts[e] = __builtin_amdgcn_readfirstlane(__hip_atomic_load(meta + e, __ATOMIC_RELAXED, __HIP_MEMORY_SCOPE_AGENT));
;         so.init(ts[8] * BM, N, G_, c_);
;     }
.LBB0_1312:
	s_or_b64 exec, exec, s[10:11]
	s_mov_b64 s[2:3], s[88:89]
	s_waitcnt lgkmcnt(0)
	s_barrier
	s_load_dwordx2 s[2:3], s[2:3], 0xf8
	v_readlane_b32 s4, v255, 4
	s_mov_b32 s1, s4
	s_mov_b32 s22, s92
	v_mov_b32_e32 v1, 0x177f0000
	s_waitcnt lgkmcnt(0)
	global_load_dword v0, v1, s[2:3] sc1
	global_load_dword v33, v1, s[2:3] offset:4 sc1
	global_load_dword v34, v1, s[2:3] offset:8 sc1
	global_load_dword v35, v1, s[2:3] offset:12 sc1
	global_load_dword v36, v1, s[2:3] offset:16 sc1
	global_load_dword v37, v1, s[2:3] offset:20 sc1
	global_load_dword v38, v1, s[2:3] offset:24 sc1
	global_load_dword v39, v1, s[2:3] offset:28 sc1
	global_load_dword v40, v1, s[2:3] offset:32 sc1
	s_mov_b32 s4, s38
	s_movk_i32 s16, 0x200
	v_readlane_b32 s5, v255, 5
	s_waitcnt vmcnt(0)
	v_readfirstlane_b32 s23, v33
	v_readfirstlane_b32 s24, v34
	v_readfirstlane_b32 s25, v35
	v_readfirstlane_b32 s26, v36
	v_readfirstlane_b32 s27, v37
	v_readfirstlane_b32 s28, v38
	v_readfirstlane_b32 s29, v39
	v_readfirstlane_b32 s30, v40
	v_mbcnt_lo_u32_b32 v0, s4, 0
	v_mbcnt_hi_u32_b32 v0, s4, v0
	s_mul_i32 s31, s30, 28
	v_add_u32_e32 v1, s93, v0
	s_cmp_lt_i32 s22, s31
	v_readfirstlane_b32 s15, v1
	s_cbranch_scc0 .LBB0_1372
	s_ashr_i32 s4, s31, 31
	s_lshr_b32 s4, s4, 29
	s_add_i32 s4, s31, s4
	s_ashr_i32 s33, s4, 3
	s_and_b32 s4, s4, -8
	s_sub_i32 s34, s31, s4
	s_ashr_i32 s4, s22, 31
	s_lshr_b32 s4, s4, 29
	s_add_i32 s7, s22, s4
	s_and_b32 s4, s7, -8
	s_sub_i32 s8, s22, s4
	s_add_i32 s35, s33, 1
	s_cmp_ge_i32 s8, s34
	s_mov_b64 s[4:5], -1
	s_cbranch_scc0 .LBB0_1315
	s_sub_i32 s5, s8, s34
	s_mul_i32 s4, s35, s34
	s_mul_i32 s5, s5, s33
	s_add_i32 s6, s4, s5
	s_mov_b64 s[4:5], 0

;     __device__ __forceinline__ bool next(int i, Unit& u) const { return so.next(i, u); }
;     __device__ __forceinline__ void setup(int G_, int c_) { so.setup(G_, c_); }
;     __device__ __forceinline__ bool next(int i, Unit& u) const { const bool ok = so.next(i >> 1, u); u.part = i & 1; return ok; }
;     __host__ __device__ bool next(int i, Unit& u) const {
;         const int L = i * G + c; if (L >= nwg) return false;
;         int wgid = L; { const int q = nwg / NXCD, r = nwg % NXCD, xcd = wgid % NXCD, off = wgid / NXCD; wgid = (xcd < r ? xcd * (q + 1) : r * (q + 1) + (xcd - r) * q) + off; }
;         const int nig = WGM * nN, gid = wgid / nig, fm = gid * WGM, gsz = (nM - fm) < WGM ? (nM - fm) : WGM;
;         u.pm = fm + ((wgid % nig) % gsz); u.pn = (wgid % nig) / gsz; u.part = 0; return true;
;     __device__ __forceinline__ void setup(int G_, int c_) {
; #pragma unroll
;         for (int e = 0; e < 9; ++e) ts[e] = __builtin_amdgcn_readfirstlane(__hip_atomic_load(meta + e, __ATOMIC_RELAXED, __HIP_MEMORY_SCOPE_AGENT));
;         so.init(ts[8] * BM, N, G_, c_);
;     }
.LBB0_1417:
	s_or_b64 exec, exec, s[10:11]
	s_mov_b64 s[2:3], s[88:89]
	s_waitcnt lgkmcnt(0)
	s_barrier
	s_load_dwordx2 s[2:3], s[2:3], 0xf8
	v_readlane_b32 s4, v255, 4
	s_mov_b32 s1, s4
	s_mov_b32 s20, s92
	v_mov_b32_e32 v1, 0x177f0000
	s_waitcnt lgkmcnt(0)
	global_load_dword v0, v1, s[2:3] sc1
	global_load_dword v33, v1, s[2:3] offset:4 sc1
	global_load_dword v34, v1, s[2:3] offset:8 sc1
	global_load_dword v35, v1, s[2:3] offset:12 sc1
	global_load_dword v36, v1, s[2:3] offset:16 sc1
	global_load_dword v37, v1, s[2:3] offset:20 sc1
	global_load_dword v38, v1, s[2:3] offset:24 sc1
	global_load_dword v39, v1, s[2:3] offset:28 sc1
	global_load_dword v40, v1, s[2:3] offset:32 sc1
	s_mov_b32 s4, s38
	s_movk_i32 s12, 0x700
	v_readlane_b32 s5, v255, 5
	s_waitcnt vmcnt(0)
	v_readfirstlane_b32 s21, v33
	v_readfirstlane_b32 s22, v34
	v_readfirstlane_b32 s23, v35
	v_readfirstlane_b32 s24, v36
	v_readfirstlane_b32 s25, v37
	v_readfirstlane_b32 s26, v38
	v_readfirstlane_b32 s27, v39
	v_readfirstlane_b32 s28, v40
	v_mbcnt_lo_u32_b32 v0, s4, 0
	v_mbcnt_hi_u32_b32 v0, s4, v0
	s_lshl_b32 s29, s28, 2
	v_add_u32_e32 v1, s93, v0
	s_cmp_lt_i32 s20, s29
	v_readfirstlane_b32 s14, v1
	s_cbranch_scc0 .LBB0_1477
	s_lshr_b32 s4, s28, 31
	s_add_i32 s4, s28, s4
	s_ashr_i32 s30, s4, 1
	s_ashr_i32 s4, s29, 31
	s_lshr_b32 s4, s4, 29
	s_add_i32 s4, s29, s4
	s_and_b32 s4, s4, -8
	s_sub_i32 s31, s29, s4
	s_ashr_i32 s4, s20, 31
	s_lshr_b32 s4, s4, 29
	s_add_i32 s7, s20, s4
	s_and_b32 s4, s7, -8
	s_sub_i32 s8, s20, s4
	s_add_i32 s33, s30, 1
	s_cmp_ge_i32 s8, s31
	s_mov_b64 s[4:5], -1
	s_cbranch_scc0 .LBB0_1420
	s_sub_i32 s5, s8, s31
	s_mul_i32 s4, s33, s31
	s_mul_i32 s5, s5, s30
	s_add_i32 s6, s5, s4
	s_mov_b64 s[4:5], 0
